# speedup vs baseline: 1.0100x; 1.0033x over previous
.Lnoprio:
	s_waitcnt vmcnt(8)
	v_cmp_ne_u32_e64 s[20:21], 0, v224
	s_add_u32 s31, s23, 1
	s_and_b32 s31, s31, 31
	s_lshl_b32 s31, s31, 8
	s_add_u32 s26, s31, s22
	s_add_u32 s31, s23, 3
	s_and_b32 s31, s31, 31
	s_mul_i32 s31, s31, 0xc0000
	s_add_u32 s24, s31, s18
	s_add_u32 s31, s23, 2
	s_and_b32 s31, s31, 31
	s_mul_i32 s31, s31, 0xc0000
	s_add_u32 s25, s31, s19
	s_cmp_eq_u64 s[20:21], -1
	s_cselect_b32 s34, s37, s38
	ds_read_b128 v[176:179], v225 offset:9216
	s_add_u32 s31, s29, 0xc00000
	buffer_load_dwordx4 v[32:35], v243, s[4:7], s31 offen nt
	s_add_u32 s31, s29, 0xc0c000
	buffer_load_dwordx4 v[36:39], v243, s[4:7], s31 offen nt
	buffer_load_dword v224, v230, s[8:11], s26 offen
	v_exp_f32_e32 v64, v64
	v_exp_f32_e32 v65, v65
	v_cvt_pk_f16_f32 v208, v208, v209
	v_cvt_pk_f16_f32 v209, v210, v211
	v_cvt_pk_f16_f32 v212, v212, v213
	v_cvt_pk_f16_f32 v213, v214, v215
	ds_write_b64 v227, v[208:209] offset:18432
	ds_write_b64 v227, v[212:213] offset:23040
	ds_read_b128 v[180:183], v225 offset:9248
	v_cvt_pk_f16_f32 v160, v64, v65
	v_add_f32_e32 v64, v64, v65
	v_exp_f32_e32 v66, v66
	v_exp_f32_e32 v67, v67
	ds_read_b128 v[184:187], v225 offset:9280
	v_cvt_pk_f16_f32 v161, v66, v67
	v_add_f32_e32 v66, v66, v67
	v_exp_f32_e32 v68, v68
	v_exp_f32_e32 v69, v69
	ds_read_b128 v[188:191], v225 offset:9312
	buffer_load_dwordx4 v[208:211], v229, s[4:7], s24 offen
	v_cvt_pk_f16_f32 v162, v68, v69
	v_add_f32_e32 v68, v68, v69
	v_add_f32_e32 v231, v64, v66
	v_exp_f32_e32 v70, v70
	v_exp_f32_e32 v71, v71
	ds_read_b128 v[192:195], v226 offset:0
	buffer_load_dwordx4 v[212:215], v252, s[4:7], s24 offen
	v_cvt_pk_f16_f32 v163, v70, v71
	v_add_f32_e32 v70, v70, v71
	v_add_f32_e32 v231, v231, v68
	v_exp_f32_e32 v72, v72
	v_exp_f32_e32 v73, v73
	ds_read_b128 v[196:199], v226 offset:4608
	v_cvt_pk_f16_f32 v164, v72, v73
	v_add_f32_e32 v72, v72, v73
	v_add_f32_e32 v231, v231, v70
	v_exp_f32_e32 v74, v74
	v_exp_f32_e32 v75, v75
	ds_read_b128 v[200:203], v226 offset:32
	v_cvt_pk_f16_f32 v165, v74, v75
	v_add_f32_e32 v74, v74, v75
	v_add_f32_e32 v231, v231, v72
	v_exp_f32_e32 v76, v76
	v_exp_f32_e32 v77, v77
	ds_read_b128 v[204:207], v226 offset:4640
	v_cvt_pk_f16_f32 v166, v76, v77
	v_add_f32_e32 v76, v76, v77
	v_add_f32_e32 v231, v231, v74
	v_exp_f32_e32 v78, v78
	v_exp_f32_e32 v79, v79
	v_add_f32_e32 v231, v231, v76
	v_cvt_pk_f16_f32 v167, v78, v79
	v_add_f32_e32 v78, v78, v79
	v_add_f32_e32 v231, v231, v78
	v_cmp_nge_f32_e32 vcc, s34, v231
	s_cbranch_vccnz .Lovf_a1_00
.Lovfret_a1_00:
	v_add_f32_e32 v232, v232, v231
	s_waitcnt lgkmcnt(4)
	v_mfma_f32_32x32x16_f16 v[64:79], v[176:179], v[128:131], v[96:111]
	ds_read_b128 v[176:179], v225 offset:13824
	s_waitcnt vmcnt(5)
	v_exp_f32_e32 v80, v80
	v_exp_f32_e32 v81, v81
	v_cvt_pk_f16_f32 v216, v216, v217
	v_cvt_pk_f16_f32 v217, v218, v219
	v_cvt_pk_f16_f32 v218, v220, v221
	v_cvt_pk_f16_f32 v219, v222, v223
	v_mfma_f32_32x32x16_f16 v[64:79], v[180:183], v[132:135], v[64:79]
	ds_write_b128 v228, v[216:219] offset:9216
	ds_read_b128 v[180:183], v225 offset:13856
	v_cvt_pk_f16_f32 v168, v80, v81
	v_add_f32_e32 v80, v80, v81
	v_exp_f32_e32 v82, v82
	v_exp_f32_e32 v83, v83
	v_mfma_f32_32x32x16_f16 v[64:79], v[184:187], v[136:139], v[64:79]
	ds_read_b128 v[184:187], v225 offset:13888
	v_cvt_pk_f16_f32 v169, v82, v83
	v_add_f32_e32 v82, v82, v83
	v_exp_f32_e32 v84, v84
	v_exp_f32_e32 v85, v85
	v_mfma_f32_32x32x16_f16 v[64:79], v[188:191], v[140:143], v[64:79]
	ds_read_b128 v[188:191], v225 offset:13920
	buffer_load_dword v216, v230, s[4:7], s25 offen
	buffer_load_dword v217, v245, s[4:7], s25 offen
	v_cvt_pk_f16_f32 v170, v84, v85
	v_add_f32_e32 v84, v84, v85
	v_add_f32_e32 v231, v80, v82
	v_exp_f32_e32 v86, v86
	v_exp_f32_e32 v87, v87
	s_waitcnt lgkmcnt(5)
	v_mfma_f32_32x32x16_f16 v[0:15], v[192:195], v[160:163], v[0:15]
	ds_read_b128 v[192:195], v226 offset:64
	buffer_load_dword v218, v246, s[4:7], s25 offen
	buffer_load_dword v219, v247, s[4:7], s25 offen
	v_cvt_pk_f16_f32 v171, v86, v87
	v_add_f32_e32 v86, v86, v87
	v_add_f32_e32 v231, v231, v84
	v_exp_f32_e32 v88, v88
	v_exp_f32_e32 v89, v89
	v_mfma_f32_32x32x16_f16 v[16:31], v[196:199], v[160:163], v[16:31]
	ds_read_b128 v[196:199], v226 offset:4672
	buffer_load_dword v220, v248, s[4:7], s25 offen
	buffer_load_dword v221, v249, s[4:7], s25 offen
	v_cvt_pk_f16_f32 v172, v88, v89
	v_add_f32_e32 v88, v88, v89
	v_add_f32_e32 v231, v231, v86
	v_exp_f32_e32 v90, v90
	v_exp_f32_e32 v91, v91
	v_mfma_f32_32x32x16_f16 v[0:15], v[200:203], v[164:167], v[0:15]
	ds_read_b128 v[200:203], v226 offset:96
	buffer_load_dword v222, v250, s[4:7], s25 offen
	v_cvt_pk_f16_f32 v173, v90, v91
	v_add_f32_e32 v90, v90, v91
	v_add_f32_e32 v231, v231, v88
	v_exp_f32_e32 v92, v92
	v_exp_f32_e32 v93, v93
	v_mfma_f32_32x32x16_f16 v[16:31], v[204:207], v[164:167], v[16:31]
	ds_read_b128 v[204:207], v226 offset:4704
	buffer_load_dword v223, v251, s[4:7], s25 offen
	v_cvt_pk_f16_f32 v174, v92, v93
	v_add_f32_e32 v92, v92, v93
	v_add_f32_e32 v231, v231, v90
	v_exp_f32_e32 v94, v94
	v_exp_f32_e32 v95, v95
	v_add_f32_e32 v231, v231, v92
	v_cvt_pk_f16_f32 v175, v94, v95
	v_add_f32_e32 v94, v94, v95
	v_add_f32_e32 v231, v231, v94
	v_cmp_nge_f32_e32 vcc, s34, v231
	s_cbranch_vccnz .Lovf_a1_01
.Lovfret_a1_01:
	v_add_f32_e32 v232, v232, v231
	s_waitcnt lgkmcnt(7)
	s_barrier
	s_add_u32 s23, s23, 1
	s_waitcnt vmcnt(8)
	v_cmp_ne_u32_e64 s[20:21], 0, v224
	s_add_u32 s31, s23, 1
	s_and_b32 s31, s31, 31
	s_lshl_b32 s31, s31, 8
	s_add_u32 s26, s31, s22
	s_add_u32 s31, s23, 3
	s_and_b32 s31, s31, 31
	s_mul_i32 s31, s31, 0xc0000
	s_add_u32 s24, s31, s18
	s_add_u32 s31, s23, 2
	s_and_b32 s31, s31, 31
	s_mul_i32 s31, s31, 0xc0000
	s_add_u32 s25, s31, s19
	s_cmp_eq_u64 s[20:21], -1
	s_cselect_b32 s34, s37, s38
	s_waitcnt lgkmcnt(4)
	v_mfma_f32_32x32x16_f16 v[80:95], v[176:179], v[128:131], v[96:111]
	ds_read_b128 v[176:179], v225 offset:18432
	s_add_u32 s31, s29, 0xc18000
	buffer_load_dwordx4 v[40:43], v243, s[4:7], s31 offen nt
	s_add_u32 s31, s29, 0xc24000
	buffer_load_dwordx4 v[44:47], v243, s[4:7], s31 offen nt
	buffer_load_dword v224, v230, s[8:11], s26 offen
	v_exp_f32_e32 v64, v64
	v_exp_f32_e32 v65, v65
	v_cvt_pk_f16_f32 v208, v208, v209
	v_cvt_pk_f16_f32 v209, v210, v211
	v_cvt_pk_f16_f32 v212, v212, v213
	v_cvt_pk_f16_f32 v213, v214, v215
	v_mfma_f32_32x32x16_f16 v[80:95], v[180:183], v[132:135], v[80:95]
	ds_write_b64 v227, v[208:209] offset:27648
	ds_write_b64 v227, v[212:213] offset:32256
	ds_read_b128 v[180:183], v225 offset:18464
	v_cvt_pk_f16_f32 v160, v64, v65
	v_add_f32_e32 v64, v64, v65
	v_exp_f32_e32 v66, v66
	v_exp_f32_e32 v67, v67
	v_mfma_f32_32x32x16_f16 v[80:95], v[184:187], v[136:139], v[80:95]
	ds_read_b128 v[184:187], v225 offset:18496
	v_cvt_pk_f16_f32 v161, v66, v67
	v_add_f32_e32 v66, v66, v67
	v_exp_f32_e32 v68, v68
	v_exp_f32_e32 v69, v69
	v_mfma_f32_32x32x16_f16 v[80:95], v[188:191], v[140:143], v[80:95]
	ds_read_b128 v[188:191], v225 offset:18528
	buffer_load_dwordx4 v[208:211], v229, s[4:7], s24 offen
	v_cvt_pk_f16_f32 v162, v68, v69
	v_add_f32_e32 v68, v68, v69
	v_add_f32_e32 v231, v64, v66
	v_exp_f32_e32 v70, v70
	v_exp_f32_e32 v71, v71
	s_waitcnt lgkmcnt(6)
	v_mfma_f32_32x32x16_f16 v[0:15], v[192:195], v[168:171], v[0:15]
	ds_read_b128 v[192:195], v226 offset:9216
	buffer_load_dwordx4 v[212:215], v252, s[4:7], s24 offen
	v_cvt_pk_f16_f32 v163, v70, v71
	v_add_f32_e32 v70, v70, v71
	v_add_f32_e32 v231, v231, v68
	v_exp_f32_e32 v72, v72
	v_exp_f32_e32 v73, v73
	v_mfma_f32_32x32x16_f16 v[16:31], v[196:199], v[168:171], v[16:31]
	ds_read_b128 v[196:199], v226 offset:13824
	v_cvt_pk_f16_f32 v164, v72, v73
	v_add_f32_e32 v72, v72, v73
	v_add_f32_e32 v231, v231, v70
	v_exp_f32_e32 v74, v74
	v_exp_f32_e32 v75, v75
	v_mfma_f32_32x32x16_f16 v[0:15], v[200:203], v[172:175], v[0:15]
	ds_read_b128 v[200:203], v226 offset:9248
	v_cvt_pk_f16_f32 v165, v74, v75
	v_add_f32_e32 v74, v74, v75
	v_add_f32_e32 v231, v231, v72
	v_exp_f32_e32 v76, v76
	v_exp_f32_e32 v77, v77
	v_mfma_f32_32x32x16_f16 v[16:31], v[204:207], v[172:175], v[16:31]
	ds_read_b128 v[204:207], v226 offset:13856
	v_cvt_pk_f16_f32 v166, v76, v77
	v_add_f32_e32 v76, v76, v77
	v_add_f32_e32 v231, v231, v74
	v_exp_f32_e32 v78, v78
	v_exp_f32_e32 v79, v79
	v_add_f32_e32 v231, v231, v76
	v_cvt_pk_f16_f32 v167, v78, v79
	v_add_f32_e32 v78, v78, v79
	v_add_f32_e32 v231, v231, v78
	v_cmp_nge_f32_e32 vcc, s34, v231
	s_cbranch_vccnz .Lovf_a1_10
.Lovfret_a1_10:
	v_add_f32_e32 v232, v232, v231
	s_waitcnt lgkmcnt(4)
	v_mfma_f32_32x32x16_f16 v[64:79], v[176:179], v[128:131], v[96:111]
	ds_read_b128 v[176:179], v225 offset:23040
	s_waitcnt vmcnt(5)
	v_exp_f32_e32 v80, v80
	v_exp_f32_e32 v81, v81
	v_cvt_pk_f16_f32 v216, v216, v217
	v_cvt_pk_f16_f32 v217, v218, v219
	v_cvt_pk_f16_f32 v218, v220, v221
	v_cvt_pk_f16_f32 v219, v222, v223
	v_mfma_f32_32x32x16_f16 v[64:79], v[180:183], v[132:135], v[64:79]
	ds_write_b128 v228, v[216:219] offset:18432
	ds_read_b128 v[180:183], v225 offset:23072
	v_cvt_pk_f16_f32 v168, v80, v81
	v_add_f32_e32 v80, v80, v81
	v_exp_f32_e32 v82, v82
	v_exp_f32_e32 v83, v83
	v_mfma_f32_32x32x16_f16 v[64:79], v[184:187], v[136:139], v[64:79]
	ds_read_b128 v[184:187], v225 offset:23104
	v_cvt_pk_f16_f32 v169, v82, v83
	v_add_f32_e32 v82, v82, v83
	v_exp_f32_e32 v84, v84
	v_exp_f32_e32 v85, v85
	v_mfma_f32_32x32x16_f16 v[64:79], v[188:191], v[140:143], v[64:79]
	ds_read_b128 v[188:191], v225 offset:23136
	buffer_load_dword v216, v230, s[4:7], s25 offen
	buffer_load_dword v217, v245, s[4:7], s25 offen
	v_cvt_pk_f16_f32 v170, v84, v85
	v_add_f32_e32 v84, v84, v85
	v_add_f32_e32 v231, v80, v82
	v_exp_f32_e32 v86, v86
	v_exp_f32_e32 v87, v87
	s_waitcnt lgkmcnt(5)
	v_mfma_f32_32x32x16_f16 v[0:15], v[192:195], v[160:163], v[0:15]
	ds_read_b128 v[192:195], v226 offset:9280
	buffer_load_dword v218, v246, s[4:7], s25 offen
	buffer_load_dword v219, v247, s[4:7], s25 offen
	v_cvt_pk_f16_f32 v171, v86, v87
	v_add_f32_e32 v86, v86, v87
	v_add_f32_e32 v231, v231, v84
	v_exp_f32_e32 v88, v88
	v_exp_f32_e32 v89, v89
	v_mfma_f32_32x32x16_f16 v[16:31], v[196:199], v[160:163], v[16:31]
	ds_read_b128 v[196:199], v226 offset:13888
	buffer_load_dword v220, v248, s[4:7], s25 offen
	buffer_load_dword v221, v249, s[4:7], s25 offen
	v_cvt_pk_f16_f32 v172, v88, v89
	v_add_f32_e32 v88, v88, v89
	v_add_f32_e32 v231, v231, v86
	v_exp_f32_e32 v90, v90
	v_exp_f32_e32 v91, v91
	v_mfma_f32_32x32x16_f16 v[0:15], v[200:203], v[164:167], v[0:15]
	ds_read_b128 v[200:203], v226 offset:9312
	buffer_load_dword v222, v250, s[4:7], s25 offen
	v_cvt_pk_f16_f32 v173, v90, v91
	v_add_f32_e32 v90, v90, v91
	v_add_f32_e32 v231, v231, v88
	v_exp_f32_e32 v92, v92
	v_exp_f32_e32 v93, v93
	v_mfma_f32_32x32x16_f16 v[16:31], v[204:207], v[164:167], v[16:31]
	ds_read_b128 v[204:207], v226 offset:13920
	buffer_load_dword v223, v251, s[4:7], s25 offen
	v_cvt_pk_f16_f32 v174, v92, v93
	v_add_f32_e32 v92, v92, v93
	v_add_f32_e32 v231, v231, v90
	v_exp_f32_e32 v94, v94
	v_exp_f32_e32 v95, v95
	v_add_f32_e32 v231, v231, v92
	v_cvt_pk_f16_f32 v175, v94, v95
	v_add_f32_e32 v94, v94, v95
	v_add_f32_e32 v231, v231, v94
	v_cmp_nge_f32_e32 vcc, s34, v231
	s_cbranch_vccnz .Lovf_a1_11
.Lovfret_a1_11:
	v_add_f32_e32 v232, v232, v231
	s_waitcnt lgkmcnt(7)
	s_barrier
	s_add_u32 s23, s23, 1
	s_waitcnt vmcnt(8)
	v_cmp_ne_u32_e64 s[20:21], 0, v224
	s_add_u32 s31, s23, 1
	s_and_b32 s31, s31, 31
	s_lshl_b32 s31, s31, 8
	s_add_u32 s26, s31, s22
	s_add_u32 s31, s23, 3
	s_and_b32 s31, s31, 31
	s_mul_i32 s31, s31, 0xc0000
	s_add_u32 s24, s31, s18
	s_add_u32 s31, s23, 2
	s_and_b32 s31, s31, 31
	s_mul_i32 s31, s31, 0xc0000
	s_add_u32 s25, s31, s19
	s_cmp_eq_u64 s[20:21], -1
	s_cselect_b32 s34, s37, s38
	s_waitcnt lgkmcnt(4)
	v_mfma_f32_32x32x16_f16 v[80:95], v[176:179], v[128:131], v[96:111]
	ds_read_b128 v[176:179], v225 offset:27648
	s_add_u32 s31, s29, 0xc30000
	buffer_load_dwordx4 v[48:51], v243, s[4:7], s31 offen nt
	s_add_u32 s31, s29, 0xc3c000
	buffer_load_dwordx4 v[52:55], v243, s[4:7], s31 offen nt
	buffer_load_dword v224, v230, s[8:11], s26 offen
	v_exp_f32_e32 v64, v64
	v_exp_f32_e32 v65, v65
	v_cvt_pk_f16_f32 v208, v208, v209
	v_cvt_pk_f16_f32 v209, v210, v211
	v_cvt_pk_f16_f32 v212, v212, v213
	v_cvt_pk_f16_f32 v213, v214, v215
	v_mfma_f32_32x32x16_f16 v[80:95], v[180:183], v[132:135], v[80:95]
	ds_write_b64 v227, v[208:209] offset:0
	ds_write_b64 v227, v[212:213] offset:4608
	ds_read_b128 v[180:183], v225 offset:27680
	v_cvt_pk_f16_f32 v160, v64, v65
	v_add_f32_e32 v64, v64, v65
	v_exp_f32_e32 v66, v66
	v_exp_f32_e32 v67, v67
	v_mfma_f32_32x32x16_f16 v[80:95], v[184:187], v[136:139], v[80:95]
	ds_read_b128 v[184:187], v225 offset:27712
	v_cvt_pk_f16_f32 v161, v66, v67
	v_add_f32_e32 v66, v66, v67
	v_exp_f32_e32 v68, v68
	v_exp_f32_e32 v69, v69
	v_mfma_f32_32x32x16_f16 v[80:95], v[188:191], v[140:143], v[80:95]
	ds_read_b128 v[188:191], v225 offset:27744
	buffer_load_dwordx4 v[208:211], v229, s[4:7], s24 offen
	v_cvt_pk_f16_f32 v162, v68, v69
	v_add_f32_e32 v68, v68, v69
	v_add_f32_e32 v231, v64, v66
	v_exp_f32_e32 v70, v70
	v_exp_f32_e32 v71, v71
	s_waitcnt lgkmcnt(6)
	v_mfma_f32_32x32x16_f16 v[0:15], v[192:195], v[168:171], v[0:15]
	ds_read_b128 v[192:195], v226 offset:18432
	buffer_load_dwordx4 v[212:215], v252, s[4:7], s24 offen
	v_cvt_pk_f16_f32 v163, v70, v71
	v_add_f32_e32 v70, v70, v71
	v_add_f32_e32 v231, v231, v68
	v_exp_f32_e32 v72, v72
	v_exp_f32_e32 v73, v73
	v_mfma_f32_32x32x16_f16 v[16:31], v[196:199], v[168:171], v[16:31]
	ds_read_b128 v[196:199], v226 offset:23040
	v_cvt_pk_f16_f32 v164, v72, v73
	v_add_f32_e32 v72, v72, v73
	v_add_f32_e32 v231, v231, v70
	v_exp_f32_e32 v74, v74
	v_exp_f32_e32 v75, v75
	v_mfma_f32_32x32x16_f16 v[0:15], v[200:203], v[172:175], v[0:15]
	ds_read_b128 v[200:203], v226 offset:18464
	v_cvt_pk_f16_f32 v165, v74, v75
	v_add_f32_e32 v74, v74, v75
	v_add_f32_e32 v231, v231, v72
	v_exp_f32_e32 v76, v76
	v_exp_f32_e32 v77, v77
	v_mfma_f32_32x32x16_f16 v[16:31], v[204:207], v[172:175], v[16:31]
	ds_read_b128 v[204:207], v226 offset:23072
	v_cvt_pk_f16_f32 v166, v76, v77
	v_add_f32_e32 v76, v76, v77
	v_add_f32_e32 v231, v231, v74
	v_exp_f32_e32 v78, v78
	v_exp_f32_e32 v79, v79
	v_add_f32_e32 v231, v231, v76
	v_cvt_pk_f16_f32 v167, v78, v79
	v_add_f32_e32 v78, v78, v79
	v_add_f32_e32 v231, v231, v78
	v_cmp_nge_f32_e32 vcc, s34, v231
	s_cbranch_vccnz .Lovf_a1_20
.Lovfret_a1_20:
	v_add_f32_e32 v232, v232, v231
	s_waitcnt lgkmcnt(4)
	v_mfma_f32_32x32x16_f16 v[64:79], v[176:179], v[128:131], v[96:111]
	ds_read_b128 v[176:179], v225 offset:32256
	s_waitcnt vmcnt(5)
	v_exp_f32_e32 v80, v80
	v_exp_f32_e32 v81, v81
	v_cvt_pk_f16_f32 v216, v216, v217
	v_cvt_pk_f16_f32 v217, v218, v219
	v_cvt_pk_f16_f32 v218, v220, v221
	v_cvt_pk_f16_f32 v219, v222, v223
	v_mfma_f32_32x32x16_f16 v[64:79], v[180:183], v[132:135], v[64:79]
	ds_write_b128 v228, v[216:219] offset:27648
	ds_read_b128 v[180:183], v225 offset:32288
	v_cvt_pk_f16_f32 v168, v80, v81
	v_add_f32_e32 v80, v80, v81
	v_exp_f32_e32 v82, v82
	v_exp_f32_e32 v83, v83
	v_mfma_f32_32x32x16_f16 v[64:79], v[184:187], v[136:139], v[64:79]
	ds_read_b128 v[184:187], v225 offset:32320
	v_cvt_pk_f16_f32 v169, v82, v83
	v_add_f32_e32 v82, v82, v83
	v_exp_f32_e32 v84, v84
	v_exp_f32_e32 v85, v85
	v_mfma_f32_32x32x16_f16 v[64:79], v[188:191], v[140:143], v[64:79]
	ds_read_b128 v[188:191], v225 offset:32352
	buffer_load_dword v216, v230, s[4:7], s25 offen
	buffer_load_dword v217, v245, s[4:7], s25 offen
	v_cvt_pk_f16_f32 v170, v84, v85
	v_add_f32_e32 v84, v84, v85
	v_add_f32_e32 v231, v80, v82
	v_exp_f32_e32 v86, v86
	v_exp_f32_e32 v87, v87
	s_waitcnt lgkmcnt(5)
	v_mfma_f32_32x32x16_f16 v[0:15], v[192:195], v[160:163], v[0:15]
	ds_read_b128 v[192:195], v226 offset:18496
	buffer_load_dword v218, v246, s[4:7], s25 offen
	buffer_load_dword v219, v247, s[4:7], s25 offen
	v_cvt_pk_f16_f32 v171, v86, v87
	v_add_f32_e32 v86, v86, v87
	v_add_f32_e32 v231, v231, v84
	v_exp_f32_e32 v88, v88
	v_exp_f32_e32 v89, v89
	v_mfma_f32_32x32x16_f16 v[16:31], v[196:199], v[160:163], v[16:31]
	ds_read_b128 v[196:199], v226 offset:23104
	buffer_load_dword v220, v248, s[4:7], s25 offen
	buffer_load_dword v221, v249, s[4:7], s25 offen
	v_cvt_pk_f16_f32 v172, v88, v89
	v_add_f32_e32 v88, v88, v89
	v_add_f32_e32 v231, v231, v86
	v_exp_f32_e32 v90, v90
	v_exp_f32_e32 v91, v91
	v_mfma_f32_32x32x16_f16 v[0:15], v[200:203], v[164:167], v[0:15]
	ds_read_b128 v[200:203], v226 offset:18528
	buffer_load_dword v222, v250, s[4:7], s25 offen
	v_cvt_pk_f16_f32 v173, v90, v91
	v_add_f32_e32 v90, v90, v91
	v_add_f32_e32 v231, v231, v88
	v_exp_f32_e32 v92, v92
	v_exp_f32_e32 v93, v93
	v_mfma_f32_32x32x16_f16 v[16:31], v[204:207], v[164:167], v[16:31]
	ds_read_b128 v[204:207], v226 offset:23136
	buffer_load_dword v223, v251, s[4:7], s25 offen
	v_cvt_pk_f16_f32 v174, v92, v93
	v_add_f32_e32 v92, v92, v93
	v_add_f32_e32 v231, v231, v90
	v_exp_f32_e32 v94, v94
	v_exp_f32_e32 v95, v95
	v_add_f32_e32 v231, v231, v92
	v_cvt_pk_f16_f32 v175, v94, v95
	v_add_f32_e32 v94, v94, v95
	v_add_f32_e32 v231, v231, v94
	v_cmp_nge_f32_e32 vcc, s34, v231
	s_cbranch_vccnz .Lovf_a1_21
.Lovfret_a1_21:
	v_add_f32_e32 v232, v232, v231
	s_waitcnt lgkmcnt(7)
	s_barrier
	s_add_u32 s23, s23, 1
	s_waitcnt vmcnt(8)
	v_cmp_ne_u32_e64 s[20:21], 0, v224
	s_add_u32 s31, s23, 1
	s_and_b32 s31, s31, 31
	s_lshl_b32 s31, s31, 8
	s_add_u32 s26, s31, s22
	s_add_u32 s31, s23, 3
	s_and_b32 s31, s31, 31
	s_mul_i32 s31, s31, 0xc0000
	s_add_u32 s24, s31, s18
	s_add_u32 s31, s23, 2
	s_and_b32 s31, s31, 31
	s_mul_i32 s31, s31, 0xc0000
	s_add_u32 s25, s31, s19
	s_cmp_eq_u64 s[20:21], -1
	s_cselect_b32 s34, s37, s38
	s_waitcnt lgkmcnt(4)
	v_mfma_f32_32x32x16_f16 v[80:95], v[176:179], v[128:131], v[96:111]
	ds_read_b128 v[176:179], v225 offset:0
	s_add_u32 s31, s29, 0xc48000
	buffer_load_dwordx4 v[56:59], v243, s[4:7], s31 offen nt
	s_add_u32 s31, s29, 0xc54000
	buffer_load_dwordx4 v[60:63], v243, s[4:7], s31 offen nt
	buffer_load_dword v224, v230, s[8:11], s26 offen
	v_exp_f32_e32 v64, v64
	v_exp_f32_e32 v65, v65
	v_cvt_pk_f16_f32 v208, v208, v209
	v_cvt_pk_f16_f32 v209, v210, v211
	v_cvt_pk_f16_f32 v212, v212, v213
	v_cvt_pk_f16_f32 v213, v214, v215
	v_mfma_f32_32x32x16_f16 v[80:95], v[180:183], v[132:135], v[80:95]
	ds_write_b64 v227, v[208:209] offset:9216
	ds_write_b64 v227, v[212:213] offset:13824
	ds_read_b128 v[180:183], v225 offset:32
	v_cvt_pk_f16_f32 v160, v64, v65
	v_add_f32_e32 v64, v64, v65
	v_exp_f32_e32 v66, v66
	v_exp_f32_e32 v67, v67
	v_mfma_f32_32x32x16_f16 v[80:95], v[184:187], v[136:139], v[80:95]
	ds_read_b128 v[184:187], v225 offset:64
	v_cvt_pk_f16_f32 v161, v66, v67
	v_add_f32_e32 v66, v66, v67
	v_exp_f32_e32 v68, v68
	v_exp_f32_e32 v69, v69
	v_mfma_f32_32x32x16_f16 v[80:95], v[188:191], v[140:143], v[80:95]
	ds_read_b128 v[188:191], v225 offset:96
	buffer_load_dwordx4 v[208:211], v229, s[4:7], s24 offen
	v_cvt_pk_f16_f32 v162, v68, v69
	v_add_f32_e32 v68, v68, v69
	v_add_f32_e32 v231, v64, v66
	v_exp_f32_e32 v70, v70
	v_exp_f32_e32 v71, v71
	s_waitcnt lgkmcnt(6)
	v_mfma_f32_32x32x16_f16 v[0:15], v[192:195], v[168:171], v[0:15]
	ds_read_b128 v[192:195], v226 offset:27648
	buffer_load_dwordx4 v[212:215], v252, s[4:7], s24 offen
	v_cvt_pk_f16_f32 v163, v70, v71
	v_add_f32_e32 v70, v70, v71
	v_add_f32_e32 v231, v231, v68
	v_exp_f32_e32 v72, v72
	v_exp_f32_e32 v73, v73
	v_mfma_f32_32x32x16_f16 v[16:31], v[196:199], v[168:171], v[16:31]
	ds_read_b128 v[196:199], v226 offset:32256
	v_cvt_pk_f16_f32 v164, v72, v73
	v_add_f32_e32 v72, v72, v73
	v_add_f32_e32 v231, v231, v70
	v_exp_f32_e32 v74, v74
	v_exp_f32_e32 v75, v75
	v_mfma_f32_32x32x16_f16 v[0:15], v[200:203], v[172:175], v[0:15]
	ds_read_b128 v[200:203], v226 offset:27680
	v_cvt_pk_f16_f32 v165, v74, v75
	v_add_f32_e32 v74, v74, v75
	v_add_f32_e32 v231, v231, v72
	v_exp_f32_e32 v76, v76
	v_exp_f32_e32 v77, v77
	v_mfma_f32_32x32x16_f16 v[16:31], v[204:207], v[172:175], v[16:31]
	ds_read_b128 v[204:207], v226 offset:32288
	v_cvt_pk_f16_f32 v166, v76, v77
	v_add_f32_e32 v76, v76, v77
	v_add_f32_e32 v231, v231, v74
	v_exp_f32_e32 v78, v78
	v_exp_f32_e32 v79, v79
	v_add_f32_e32 v231, v231, v76
	v_cvt_pk_f16_f32 v167, v78, v79
	v_add_f32_e32 v78, v78, v79
	v_add_f32_e32 v231, v231, v78
	v_cmp_nge_f32_e32 vcc, s34, v231
	s_cbranch_vccnz .Lovf_a1_30
.Lovfret_a1_30:
	v_add_f32_e32 v232, v232, v231
	s_waitcnt lgkmcnt(4)
	v_mfma_f32_32x32x16_f16 v[64:79], v[176:179], v[128:131], v[96:111]
	s_waitcnt vmcnt(5)
	v_exp_f32_e32 v80, v80
	v_exp_f32_e32 v81, v81
	v_cvt_pk_f16_f32 v216, v216, v217
	v_cvt_pk_f16_f32 v217, v218, v219
	v_cvt_pk_f16_f32 v218, v220, v221
	v_cvt_pk_f16_f32 v219, v222, v223
	v_mfma_f32_32x32x16_f16 v[64:79], v[180:183], v[132:135], v[64:79]
	ds_write_b128 v228, v[216:219] offset:0
	v_cvt_pk_f16_f32 v168, v80, v81
	v_add_f32_e32 v80, v80, v81
	v_exp_f32_e32 v82, v82
	v_exp_f32_e32 v83, v83
	v_mfma_f32_32x32x16_f16 v[64:79], v[184:187], v[136:139], v[64:79]
	v_cvt_pk_f16_f32 v169, v82, v83
	v_add_f32_e32 v82, v82, v83
	v_exp_f32_e32 v84, v84
	v_exp_f32_e32 v85, v85
	v_mfma_f32_32x32x16_f16 v[64:79], v[188:191], v[140:143], v[64:79]
	buffer_load_dword v216, v230, s[4:7], s25 offen
	buffer_load_dword v217, v245, s[4:7], s25 offen
	v_cvt_pk_f16_f32 v170, v84, v85
	v_add_f32_e32 v84, v84, v85
	v_add_f32_e32 v231, v80, v82
	v_exp_f32_e32 v86, v86
	v_exp_f32_e32 v87, v87
	s_waitcnt lgkmcnt(1)
	v_mfma_f32_32x32x16_f16 v[0:15], v[192:195], v[160:163], v[0:15]
	ds_read_b128 v[192:195], v226 offset:27712
	buffer_load_dword v218, v246, s[4:7], s25 offen
	buffer_load_dword v219, v247, s[4:7], s25 offen
	v_cvt_pk_f16_f32 v171, v86, v87
	v_add_f32_e32 v86, v86, v87
	v_add_f32_e32 v231, v231, v84
	v_exp_f32_e32 v88, v88
	v_exp_f32_e32 v89, v89
	v_mfma_f32_32x32x16_f16 v[16:31], v[196:199], v[160:163], v[16:31]
	ds_read_b128 v[196:199], v226 offset:32320
	buffer_load_dword v220, v248, s[4:7], s25 offen
	buffer_load_dword v221, v249, s[4:7], s25 offen
	v_cvt_pk_f16_f32 v172, v88, v89
	v_add_f32_e32 v88, v88, v89
	v_add_f32_e32 v231, v231, v86
	v_exp_f32_e32 v90, v90
	v_exp_f32_e32 v91, v91
	v_mfma_f32_32x32x16_f16 v[0:15], v[200:203], v[164:167], v[0:15]
	ds_read_b128 v[200:203], v226 offset:27744
	buffer_load_dword v222, v250, s[4:7], s25 offen
	v_cvt_pk_f16_f32 v173, v90, v91
	v_add_f32_e32 v90, v90, v91
	v_add_f32_e32 v231, v231, v88
	v_exp_f32_e32 v92, v92
	v_exp_f32_e32 v93, v93
	v_mfma_f32_32x32x16_f16 v[16:31], v[204:207], v[164:167], v[16:31]
	ds_read_b128 v[204:207], v226 offset:32352
	buffer_load_dword v223, v251, s[4:7], s25 offen
	v_cvt_pk_f16_f32 v174, v92, v93
	v_add_f32_e32 v92, v92, v93
	v_add_f32_e32 v231, v231, v90
	v_exp_f32_e32 v94, v94
	v_exp_f32_e32 v95, v95
	v_add_f32_e32 v231, v231, v92
	v_cvt_pk_f16_f32 v175, v94, v95
	v_add_f32_e32 v94, v94, v95
	v_add_f32_e32 v231, v231, v94
	v_cmp_nge_f32_e32 vcc, s34, v231
	s_cbranch_vccnz .Lovf_a1_31

.Lbody:
	s_waitcnt lgkmcnt(0)
	v_mfma_f32_32x32x16_f16 v[80:95], v[176:179], v[144:147], v[112:127]
	s_waitcnt vmcnt(8)
	v_cmp_ne_u32_e64 s[20:21], 0, v224
	s_add_u32 s31, s23, 1
	s_and_b32 s31, s31, 31
	s_lshl_b32 s31, s31, 8
	s_add_u32 s26, s31, s22
	s_add_u32 s31, s23, 3
	s_and_b32 s31, s31, 31
	s_mul_i32 s31, s31, 0xc0000
	s_add_u32 s24, s31, s18
	s_add_u32 s31, s23, 2
	s_and_b32 s31, s31, 31
	s_mul_i32 s31, s31, 0xc0000
	s_add_u32 s25, s31, s19
	s_cmp_eq_u64 s[20:21], -1
	s_cselect_b32 s34, s37, s38
	ds_read_b128 v[176:179], v225 offset:4608
	buffer_load_dword v224, v230, s[8:11], s26 offen
	v_exp_f32_e32 v64, v64
	v_exp_f32_e32 v65, v65
	v_cvt_pk_f16_f32 v208, v208, v209
	v_cvt_pk_f16_f32 v209, v210, v211
	v_cvt_pk_f16_f32 v212, v212, v213
	v_cvt_pk_f16_f32 v213, v214, v215
	v_mfma_f32_32x32x16_f16 v[80:95], v[180:183], v[148:151], v[80:95]
	ds_write_b64 v227, v[208:209] offset:18432
	ds_write_b64 v227, v[212:213] offset:23040
	ds_read_b128 v[180:183], v225 offset:4640
	v_cvt_pk_f16_f32 v160, v64, v65
	v_add_f32_e32 v64, v64, v65
	v_exp_f32_e32 v66, v66
	v_exp_f32_e32 v67, v67
	v_mfma_f32_32x32x16_f16 v[80:95], v[184:187], v[152:155], v[80:95]
	ds_read_b128 v[184:187], v225 offset:4672
	v_cvt_pk_f16_f32 v161, v66, v67
	v_add_f32_e32 v66, v66, v67
	v_exp_f32_e32 v68, v68
	v_exp_f32_e32 v69, v69
	v_mfma_f32_32x32x16_f16 v[80:95], v[188:191], v[156:159], v[80:95]
	ds_read_b128 v[188:191], v225 offset:4704
	v_cvt_pk_f16_f32 v162, v68, v69
	v_add_f32_e32 v68, v68, v69
	v_add_f32_e32 v231, v64, v66
	v_exp_f32_e32 v70, v70
	v_exp_f32_e32 v71, v71
	v_mfma_f32_32x32x16_f16 v[32:47], v[192:195], v[168:171], v[32:47]
	ds_read_b128 v[192:195], v226 offset:0
	v_cvt_pk_f16_f32 v163, v70, v71
	v_add_f32_e32 v70, v70, v71
	v_add_f32_e32 v231, v231, v68
	v_exp_f32_e32 v72, v72
	v_exp_f32_e32 v73, v73
	v_mfma_f32_32x32x16_f16 v[48:63], v[196:199], v[168:171], v[48:63]
	ds_read_b128 v[196:199], v226 offset:4608
	v_cvt_pk_f16_f32 v164, v72, v73
	v_add_f32_e32 v72, v72, v73
	v_add_f32_e32 v231, v231, v70
	v_exp_f32_e32 v74, v74
	v_exp_f32_e32 v75, v75
	v_mfma_f32_32x32x16_f16 v[32:47], v[200:203], v[172:175], v[32:47]
	ds_read_b128 v[200:203], v226 offset:32
	v_cvt_pk_f16_f32 v165, v74, v75
	v_add_f32_e32 v74, v74, v75
	v_add_f32_e32 v231, v231, v72
	v_exp_f32_e32 v76, v76
	v_exp_f32_e32 v77, v77
	v_mfma_f32_32x32x16_f16 v[48:63], v[204:207], v[172:175], v[48:63]
	ds_read_b128 v[204:207], v226 offset:4640
	v_cvt_pk_f16_f32 v166, v76, v77
	v_add_f32_e32 v76, v76, v77
	v_add_f32_e32 v231, v231, v74
	v_exp_f32_e32 v78, v78
	v_exp_f32_e32 v79, v79
	v_add_f32_e32 v231, v231, v76
	v_cvt_pk_f16_f32 v167, v78, v79
	v_add_f32_e32 v78, v78, v79
	v_add_f32_e32 v231, v231, v78
	v_cmp_nge_f32_e32 vcc, s34, v231
	s_cbranch_vccnz .Lovf_a00

.Lovfret_b00:
	v_add_f32_e32 v233, v233, v231
	s_waitcnt lgkmcnt(0)
	v_mfma_f32_32x32x16_f16 v[80:95], v[176:179], v[144:147], v[112:127]
	ds_read_b128 v[176:179], v225 offset:9216
	s_waitcnt vmcnt(3)
	v_exp_f32_e32 v64, v64
	v_exp_f32_e32 v65, v65
	v_cvt_pk_f16_f32 v216, v216, v217
	v_cvt_pk_f16_f32 v217, v218, v219
	v_cvt_pk_f16_f32 v218, v220, v221
	v_cvt_pk_f16_f32 v219, v222, v223
	v_mfma_f32_32x32x16_f16 v[80:95], v[180:183], v[148:151], v[80:95]
	ds_write_b128 v228, v[216:219] offset:9216
	ds_read_b128 v[180:183], v225 offset:9248
	v_cvt_pk_f16_f32 v160, v64, v65
	v_add_f32_e32 v64, v64, v65
	v_exp_f32_e32 v66, v66
	v_exp_f32_e32 v67, v67
	v_mfma_f32_32x32x16_f16 v[80:95], v[184:187], v[152:155], v[80:95]
	ds_read_b128 v[184:187], v225 offset:9280
	v_cvt_pk_f16_f32 v161, v66, v67
	v_add_f32_e32 v66, v66, v67
	v_exp_f32_e32 v68, v68
	v_exp_f32_e32 v69, v69
	v_mfma_f32_32x32x16_f16 v[80:95], v[188:191], v[156:159], v[80:95]
	ds_read_b128 v[188:191], v225 offset:9312
	v_cvt_pk_f16_f32 v162, v68, v69
	v_add_f32_e32 v68, v68, v69
	v_add_f32_e32 v231, v64, v66
	v_exp_f32_e32 v70, v70
	v_exp_f32_e32 v71, v71
	v_mfma_f32_32x32x16_f16 v[32:47], v[192:195], v[168:171], v[32:47]
	ds_read_b128 v[192:195], v226 offset:64
	v_cvt_pk_f16_f32 v163, v70, v71
	v_add_f32_e32 v70, v70, v71
	v_add_f32_e32 v231, v231, v68
	v_exp_f32_e32 v72, v72
	v_exp_f32_e32 v73, v73
	v_mfma_f32_32x32x16_f16 v[48:63], v[196:199], v[168:171], v[48:63]
	ds_read_b128 v[196:199], v226 offset:4672
	v_cvt_pk_f16_f32 v164, v72, v73
	v_add_f32_e32 v72, v72, v73
	v_add_f32_e32 v231, v231, v70
	v_exp_f32_e32 v74, v74
	v_exp_f32_e32 v75, v75
	v_mfma_f32_32x32x16_f16 v[32:47], v[200:203], v[172:175], v[32:47]
	ds_read_b128 v[200:203], v226 offset:96
	v_cvt_pk_f16_f32 v165, v74, v75
	v_add_f32_e32 v74, v74, v75
	v_add_f32_e32 v231, v231, v72
	v_exp_f32_e32 v76, v76
	v_exp_f32_e32 v77, v77
	v_mfma_f32_32x32x16_f16 v[48:63], v[204:207], v[172:175], v[48:63]
	ds_read_b128 v[204:207], v226 offset:4704
	v_cvt_pk_f16_f32 v166, v76, v77
	v_add_f32_e32 v76, v76, v77
	v_add_f32_e32 v231, v231, v74
	v_exp_f32_e32 v78, v78
	v_exp_f32_e32 v79, v79
	v_add_f32_e32 v231, v231, v76
	v_cvt_pk_f16_f32 v167, v78, v79
	v_add_f32_e32 v78, v78, v79
	v_add_f32_e32 v231, v231, v78
	v_cmp_nge_f32_e32 vcc, s34, v231
	s_cbranch_vccnz .Lovf_a01

.Lovfret_b01:
	v_add_f32_e32 v233, v233, v231
	s_waitcnt lgkmcnt(7)
	s_barrier
	s_add_u32 s23, s23, 1
	s_waitcnt lgkmcnt(0)
	v_mfma_f32_32x32x16_f16 v[80:95], v[176:179], v[144:147], v[112:127]
	s_waitcnt vmcnt(8)
	v_cmp_ne_u32_e64 s[20:21], 0, v224
	s_add_u32 s31, s23, 1
	s_and_b32 s31, s31, 31
	s_lshl_b32 s31, s31, 8
	s_add_u32 s26, s31, s22
	s_add_u32 s31, s23, 3
	s_and_b32 s31, s31, 31
	s_mul_i32 s31, s31, 0xc0000
	s_add_u32 s24, s31, s18
	s_add_u32 s31, s23, 2
	s_and_b32 s31, s31, 31
	s_mul_i32 s31, s31, 0xc0000
	s_add_u32 s25, s31, s19
	s_cmp_eq_u64 s[20:21], -1
	s_cselect_b32 s34, s37, s38
	ds_read_b128 v[176:179], v225 offset:13824
	buffer_load_dword v224, v230, s[8:11], s26 offen
	v_exp_f32_e32 v64, v64
	v_exp_f32_e32 v65, v65
	v_cvt_pk_f16_f32 v208, v208, v209
	v_cvt_pk_f16_f32 v209, v210, v211
	v_cvt_pk_f16_f32 v212, v212, v213
	v_cvt_pk_f16_f32 v213, v214, v215
	v_mfma_f32_32x32x16_f16 v[80:95], v[180:183], v[148:151], v[80:95]
	ds_write_b64 v227, v[208:209] offset:27648
	ds_write_b64 v227, v[212:213] offset:32256
	ds_read_b128 v[180:183], v225 offset:13856
	v_cvt_pk_f16_f32 v160, v64, v65
	v_add_f32_e32 v64, v64, v65
	v_exp_f32_e32 v66, v66
	v_exp_f32_e32 v67, v67
	v_mfma_f32_32x32x16_f16 v[80:95], v[184:187], v[152:155], v[80:95]
	ds_read_b128 v[184:187], v225 offset:13888
	v_cvt_pk_f16_f32 v161, v66, v67
	v_add_f32_e32 v66, v66, v67
	v_exp_f32_e32 v68, v68
	v_exp_f32_e32 v69, v69
	v_mfma_f32_32x32x16_f16 v[80:95], v[188:191], v[156:159], v[80:95]
	ds_read_b128 v[188:191], v225 offset:13920
	v_cvt_pk_f16_f32 v162, v68, v69
	v_add_f32_e32 v68, v68, v69
	v_add_f32_e32 v231, v64, v66
	v_exp_f32_e32 v70, v70
	v_exp_f32_e32 v71, v71
	v_mfma_f32_32x32x16_f16 v[32:47], v[192:195], v[168:171], v[32:47]
	ds_read_b128 v[192:195], v226 offset:9216
	v_cvt_pk_f16_f32 v163, v70, v71
	v_add_f32_e32 v70, v70, v71
	v_add_f32_e32 v231, v231, v68
	v_exp_f32_e32 v72, v72
	v_exp_f32_e32 v73, v73
	v_mfma_f32_32x32x16_f16 v[48:63], v[196:199], v[168:171], v[48:63]
	ds_read_b128 v[196:199], v226 offset:13824
	v_cvt_pk_f16_f32 v164, v72, v73
	v_add_f32_e32 v72, v72, v73
	v_add_f32_e32 v231, v231, v70
	v_exp_f32_e32 v74, v74
	v_exp_f32_e32 v75, v75
	v_mfma_f32_32x32x16_f16 v[32:47], v[200:203], v[172:175], v[32:47]
	ds_read_b128 v[200:203], v226 offset:9248
	v_cvt_pk_f16_f32 v165, v74, v75
	v_add_f32_e32 v74, v74, v75
	v_add_f32_e32 v231, v231, v72
	v_exp_f32_e32 v76, v76
	v_exp_f32_e32 v77, v77
	v_mfma_f32_32x32x16_f16 v[48:63], v[204:207], v[172:175], v[48:63]
	ds_read_b128 v[204:207], v226 offset:13856
	v_cvt_pk_f16_f32 v166, v76, v77
	v_add_f32_e32 v76, v76, v77
	v_add_f32_e32 v231, v231, v74
	v_exp_f32_e32 v78, v78
	v_exp_f32_e32 v79, v79
	v_add_f32_e32 v231, v231, v76
	v_cvt_pk_f16_f32 v167, v78, v79
	v_add_f32_e32 v78, v78, v79
	v_add_f32_e32 v231, v231, v78
	v_cmp_nge_f32_e32 vcc, s34, v231
	s_cbranch_vccnz .Lovf_a10

.Lovfret_b10:
	v_add_f32_e32 v233, v233, v231
	s_waitcnt lgkmcnt(0)
	v_mfma_f32_32x32x16_f16 v[80:95], v[176:179], v[144:147], v[112:127]
	ds_read_b128 v[176:179], v225 offset:18432
	s_waitcnt vmcnt(3)
	v_exp_f32_e32 v64, v64
	v_exp_f32_e32 v65, v65
	v_cvt_pk_f16_f32 v216, v216, v217
	v_cvt_pk_f16_f32 v217, v218, v219
	v_cvt_pk_f16_f32 v218, v220, v221
	v_cvt_pk_f16_f32 v219, v222, v223
	v_mfma_f32_32x32x16_f16 v[80:95], v[180:183], v[148:151], v[80:95]
	ds_write_b128 v228, v[216:219] offset:18432
	ds_read_b128 v[180:183], v225 offset:18464
	v_cvt_pk_f16_f32 v160, v64, v65
	v_add_f32_e32 v64, v64, v65
	v_exp_f32_e32 v66, v66
	v_exp_f32_e32 v67, v67
	v_mfma_f32_32x32x16_f16 v[80:95], v[184:187], v[152:155], v[80:95]
	ds_read_b128 v[184:187], v225 offset:18496
	v_cvt_pk_f16_f32 v161, v66, v67
	v_add_f32_e32 v66, v66, v67
	v_exp_f32_e32 v68, v68
	v_exp_f32_e32 v69, v69
	v_mfma_f32_32x32x16_f16 v[80:95], v[188:191], v[156:159], v[80:95]
	ds_read_b128 v[188:191], v225 offset:18528
	v_cvt_pk_f16_f32 v162, v68, v69
	v_add_f32_e32 v68, v68, v69
	v_add_f32_e32 v231, v64, v66
	v_exp_f32_e32 v70, v70
	v_exp_f32_e32 v71, v71
	v_mfma_f32_32x32x16_f16 v[32:47], v[192:195], v[168:171], v[32:47]
	ds_read_b128 v[192:195], v226 offset:9280
	v_cvt_pk_f16_f32 v163, v70, v71
	v_add_f32_e32 v70, v70, v71
	v_add_f32_e32 v231, v231, v68
	v_exp_f32_e32 v72, v72
	v_exp_f32_e32 v73, v73
	v_mfma_f32_32x32x16_f16 v[48:63], v[196:199], v[168:171], v[48:63]
	ds_read_b128 v[196:199], v226 offset:13888
	v_cvt_pk_f16_f32 v164, v72, v73
	v_add_f32_e32 v72, v72, v73
	v_add_f32_e32 v231, v231, v70
	v_exp_f32_e32 v74, v74
	v_exp_f32_e32 v75, v75
	v_mfma_f32_32x32x16_f16 v[32:47], v[200:203], v[172:175], v[32:47]
	ds_read_b128 v[200:203], v226 offset:9312
	v_cvt_pk_f16_f32 v165, v74, v75
	v_add_f32_e32 v74, v74, v75
	v_add_f32_e32 v231, v231, v72
	v_exp_f32_e32 v76, v76
	v_exp_f32_e32 v77, v77
	v_mfma_f32_32x32x16_f16 v[48:63], v[204:207], v[172:175], v[48:63]
	ds_read_b128 v[204:207], v226 offset:13920
	v_cvt_pk_f16_f32 v166, v76, v77
	v_add_f32_e32 v76, v76, v77
	v_add_f32_e32 v231, v231, v74
	v_exp_f32_e32 v78, v78
	v_exp_f32_e32 v79, v79
	v_add_f32_e32 v231, v231, v76
	v_cvt_pk_f16_f32 v167, v78, v79
	v_add_f32_e32 v78, v78, v79
	v_add_f32_e32 v231, v231, v78
	v_cmp_nge_f32_e32 vcc, s34, v231
	s_cbranch_vccnz .Lovf_a11

.Lovfret_b11:
	v_add_f32_e32 v233, v233, v231
	s_waitcnt lgkmcnt(7)
	s_barrier
	s_add_u32 s23, s23, 1
	s_waitcnt lgkmcnt(0)
	v_mfma_f32_32x32x16_f16 v[80:95], v[176:179], v[144:147], v[112:127]
	s_waitcnt vmcnt(8)
	v_cmp_ne_u32_e64 s[20:21], 0, v224
	s_add_u32 s31, s23, 1
	s_and_b32 s31, s31, 31
	s_lshl_b32 s31, s31, 8
	s_add_u32 s26, s31, s22
	s_add_u32 s31, s23, 3
	s_and_b32 s31, s31, 31
	s_mul_i32 s31, s31, 0xc0000
	s_add_u32 s24, s31, s18
	s_add_u32 s31, s23, 2
	s_and_b32 s31, s31, 31
	s_mul_i32 s31, s31, 0xc0000
	s_add_u32 s25, s31, s19
	s_cmp_eq_u64 s[20:21], -1
	s_cselect_b32 s34, s37, s38
	ds_read_b128 v[176:179], v225 offset:23040
	buffer_load_dword v224, v230, s[8:11], s26 offen
	v_exp_f32_e32 v64, v64
	v_exp_f32_e32 v65, v65
	v_cvt_pk_f16_f32 v208, v208, v209
	v_cvt_pk_f16_f32 v209, v210, v211
	v_cvt_pk_f16_f32 v212, v212, v213
	v_cvt_pk_f16_f32 v213, v214, v215
	v_mfma_f32_32x32x16_f16 v[80:95], v[180:183], v[148:151], v[80:95]
	ds_write_b64 v227, v[208:209] offset:0
	ds_write_b64 v227, v[212:213] offset:4608
	ds_read_b128 v[180:183], v225 offset:23072
	v_cvt_pk_f16_f32 v160, v64, v65
	v_add_f32_e32 v64, v64, v65
	v_exp_f32_e32 v66, v66
	v_exp_f32_e32 v67, v67
	v_mfma_f32_32x32x16_f16 v[80:95], v[184:187], v[152:155], v[80:95]
	ds_read_b128 v[184:187], v225 offset:23104
	v_cvt_pk_f16_f32 v161, v66, v67
	v_add_f32_e32 v66, v66, v67
	v_exp_f32_e32 v68, v68
	v_exp_f32_e32 v69, v69
	v_mfma_f32_32x32x16_f16 v[80:95], v[188:191], v[156:159], v[80:95]
	ds_read_b128 v[188:191], v225 offset:23136
	v_cvt_pk_f16_f32 v162, v68, v69
	v_add_f32_e32 v68, v68, v69
	v_add_f32_e32 v231, v64, v66
	v_exp_f32_e32 v70, v70
	v_exp_f32_e32 v71, v71
	v_mfma_f32_32x32x16_f16 v[32:47], v[192:195], v[168:171], v[32:47]
	ds_read_b128 v[192:195], v226 offset:18432
	v_cvt_pk_f16_f32 v163, v70, v71
	v_add_f32_e32 v70, v70, v71
	v_add_f32_e32 v231, v231, v68
	v_exp_f32_e32 v72, v72
	v_exp_f32_e32 v73, v73
	v_mfma_f32_32x32x16_f16 v[48:63], v[196:199], v[168:171], v[48:63]
	ds_read_b128 v[196:199], v226 offset:23040
	v_cvt_pk_f16_f32 v164, v72, v73
	v_add_f32_e32 v72, v72, v73
	v_add_f32_e32 v231, v231, v70
	v_exp_f32_e32 v74, v74
	v_exp_f32_e32 v75, v75
	v_mfma_f32_32x32x16_f16 v[32:47], v[200:203], v[172:175], v[32:47]
	ds_read_b128 v[200:203], v226 offset:18464
	v_cvt_pk_f16_f32 v165, v74, v75
	v_add_f32_e32 v74, v74, v75
	v_add_f32_e32 v231, v231, v72
	v_exp_f32_e32 v76, v76
	v_exp_f32_e32 v77, v77
	v_mfma_f32_32x32x16_f16 v[48:63], v[204:207], v[172:175], v[48:63]
	ds_read_b128 v[204:207], v226 offset:23072
	v_cvt_pk_f16_f32 v166, v76, v77
	v_add_f32_e32 v76, v76, v77
	v_add_f32_e32 v231, v231, v74
	v_exp_f32_e32 v78, v78
	v_exp_f32_e32 v79, v79
	v_add_f32_e32 v231, v231, v76
	v_cvt_pk_f16_f32 v167, v78, v79
	v_add_f32_e32 v78, v78, v79
	v_add_f32_e32 v231, v231, v78
	v_cmp_nge_f32_e32 vcc, s34, v231
	s_cbranch_vccnz .Lovf_a20

.Lovfret_b20:
	v_add_f32_e32 v233, v233, v231
	s_waitcnt lgkmcnt(0)
	v_mfma_f32_32x32x16_f16 v[80:95], v[176:179], v[144:147], v[112:127]
	ds_read_b128 v[176:179], v225 offset:27648
	s_waitcnt vmcnt(3)
	v_exp_f32_e32 v64, v64
	v_exp_f32_e32 v65, v65
	v_cvt_pk_f16_f32 v216, v216, v217
	v_cvt_pk_f16_f32 v217, v218, v219
	v_cvt_pk_f16_f32 v218, v220, v221
	v_cvt_pk_f16_f32 v219, v222, v223
	v_mfma_f32_32x32x16_f16 v[80:95], v[180:183], v[148:151], v[80:95]
	ds_write_b128 v228, v[216:219] offset:27648
	ds_read_b128 v[180:183], v225 offset:27680
	v_cvt_pk_f16_f32 v160, v64, v65
	v_add_f32_e32 v64, v64, v65
	v_exp_f32_e32 v66, v66
	v_exp_f32_e32 v67, v67
	v_mfma_f32_32x32x16_f16 v[80:95], v[184:187], v[152:155], v[80:95]
	ds_read_b128 v[184:187], v225 offset:27712
	v_cvt_pk_f16_f32 v161, v66, v67
	v_add_f32_e32 v66, v66, v67
	v_exp_f32_e32 v68, v68
	v_exp_f32_e32 v69, v69
	v_mfma_f32_32x32x16_f16 v[80:95], v[188:191], v[156:159], v[80:95]
	ds_read_b128 v[188:191], v225 offset:27744
	v_cvt_pk_f16_f32 v162, v68, v69
	v_add_f32_e32 v68, v68, v69
	v_add_f32_e32 v231, v64, v66
	v_exp_f32_e32 v70, v70
	v_exp_f32_e32 v71, v71
	v_mfma_f32_32x32x16_f16 v[32:47], v[192:195], v[168:171], v[32:47]
	ds_read_b128 v[192:195], v226 offset:18496
	v_cvt_pk_f16_f32 v163, v70, v71
	v_add_f32_e32 v70, v70, v71
	v_add_f32_e32 v231, v231, v68
	v_exp_f32_e32 v72, v72
	v_exp_f32_e32 v73, v73
	v_mfma_f32_32x32x16_f16 v[48:63], v[196:199], v[168:171], v[48:63]
	ds_read_b128 v[196:199], v226 offset:23104
	v_cvt_pk_f16_f32 v164, v72, v73
	v_add_f32_e32 v72, v72, v73
	v_add_f32_e32 v231, v231, v70
	v_exp_f32_e32 v74, v74
	v_exp_f32_e32 v75, v75
	v_mfma_f32_32x32x16_f16 v[32:47], v[200:203], v[172:175], v[32:47]
	ds_read_b128 v[200:203], v226 offset:18528
	v_cvt_pk_f16_f32 v165, v74, v75
	v_add_f32_e32 v74, v74, v75
	v_add_f32_e32 v231, v231, v72
	v_exp_f32_e32 v76, v76
	v_exp_f32_e32 v77, v77
	v_mfma_f32_32x32x16_f16 v[48:63], v[204:207], v[172:175], v[48:63]
	ds_read_b128 v[204:207], v226 offset:23136
	v_cvt_pk_f16_f32 v166, v76, v77
	v_add_f32_e32 v76, v76, v77
	v_add_f32_e32 v231, v231, v74
	v_exp_f32_e32 v78, v78
	v_exp_f32_e32 v79, v79
	v_add_f32_e32 v231, v231, v76
	v_cvt_pk_f16_f32 v167, v78, v79
	v_add_f32_e32 v78, v78, v79
	v_add_f32_e32 v231, v231, v78
	v_cmp_nge_f32_e32 vcc, s34, v231
	s_cbranch_vccnz .Lovf_a21

.Lovfret_b21:
	v_add_f32_e32 v233, v233, v231
	s_waitcnt lgkmcnt(7)
	s_barrier
	s_add_u32 s23, s23, 1
	s_waitcnt lgkmcnt(0)
	v_mfma_f32_32x32x16_f16 v[80:95], v[176:179], v[144:147], v[112:127]
	s_waitcnt vmcnt(8)
	v_cmp_ne_u32_e64 s[20:21], 0, v224
	s_add_u32 s31, s23, 1
	s_and_b32 s31, s31, 31
	s_lshl_b32 s31, s31, 8
	s_add_u32 s26, s31, s22
	s_add_u32 s31, s23, 3
	s_and_b32 s31, s31, 31
	s_mul_i32 s31, s31, 0xc0000
	s_add_u32 s24, s31, s18
	s_add_u32 s31, s23, 2
	s_and_b32 s31, s31, 31
	s_mul_i32 s31, s31, 0xc0000
	s_add_u32 s25, s31, s19
	s_cmp_eq_u64 s[20:21], -1
	s_cselect_b32 s34, s37, s38
	ds_read_b128 v[176:179], v225 offset:32256
	buffer_load_dword v224, v230, s[8:11], s26 offen
	v_exp_f32_e32 v64, v64
	v_exp_f32_e32 v65, v65
	v_cvt_pk_f16_f32 v208, v208, v209
	v_cvt_pk_f16_f32 v209, v210, v211
	v_cvt_pk_f16_f32 v212, v212, v213
	v_cvt_pk_f16_f32 v213, v214, v215
	v_mfma_f32_32x32x16_f16 v[80:95], v[180:183], v[148:151], v[80:95]
	ds_write_b64 v227, v[208:209] offset:9216
	ds_write_b64 v227, v[212:213] offset:13824
	ds_read_b128 v[180:183], v225 offset:32288
	v_cvt_pk_f16_f32 v160, v64, v65
	v_add_f32_e32 v64, v64, v65
	v_exp_f32_e32 v66, v66
	v_exp_f32_e32 v67, v67
	v_mfma_f32_32x32x16_f16 v[80:95], v[184:187], v[152:155], v[80:95]
	ds_read_b128 v[184:187], v225 offset:32320
	v_cvt_pk_f16_f32 v161, v66, v67
	v_add_f32_e32 v66, v66, v67
	v_exp_f32_e32 v68, v68
	v_exp_f32_e32 v69, v69
	v_mfma_f32_32x32x16_f16 v[80:95], v[188:191], v[156:159], v[80:95]
	ds_read_b128 v[188:191], v225 offset:32352
	v_cvt_pk_f16_f32 v162, v68, v69
	v_add_f32_e32 v68, v68, v69
	v_add_f32_e32 v231, v64, v66
	v_exp_f32_e32 v70, v70
	v_exp_f32_e32 v71, v71
	v_mfma_f32_32x32x16_f16 v[32:47], v[192:195], v[168:171], v[32:47]
	ds_read_b128 v[192:195], v226 offset:27648
	v_cvt_pk_f16_f32 v163, v70, v71
	v_add_f32_e32 v70, v70, v71
	v_add_f32_e32 v231, v231, v68
	v_exp_f32_e32 v72, v72
	v_exp_f32_e32 v73, v73
	v_mfma_f32_32x32x16_f16 v[48:63], v[196:199], v[168:171], v[48:63]
	ds_read_b128 v[196:199], v226 offset:32256
	v_cvt_pk_f16_f32 v164, v72, v73
	v_add_f32_e32 v72, v72, v73
	v_add_f32_e32 v231, v231, v70
	v_exp_f32_e32 v74, v74
	v_exp_f32_e32 v75, v75
	v_mfma_f32_32x32x16_f16 v[32:47], v[200:203], v[172:175], v[32:47]
	ds_read_b128 v[200:203], v226 offset:27680
	v_cvt_pk_f16_f32 v165, v74, v75
	v_add_f32_e32 v74, v74, v75
	v_add_f32_e32 v231, v231, v72
	v_exp_f32_e32 v76, v76
	v_exp_f32_e32 v77, v77
	v_mfma_f32_32x32x16_f16 v[48:63], v[204:207], v[172:175], v[48:63]
	ds_read_b128 v[204:207], v226 offset:32288
	v_cvt_pk_f16_f32 v166, v76, v77
	v_add_f32_e32 v76, v76, v77
	v_add_f32_e32 v231, v231, v74
	v_exp_f32_e32 v78, v78
	v_exp_f32_e32 v79, v79
	v_add_f32_e32 v231, v231, v76
	v_cvt_pk_f16_f32 v167, v78, v79
	v_add_f32_e32 v78, v78, v79
	v_add_f32_e32 v231, v231, v78
	v_cmp_nge_f32_e32 vcc, s34, v231
	s_cbranch_vccnz .Lovf_a30

.Lovfret_b30:
	v_add_f32_e32 v233, v233, v231
	s_waitcnt lgkmcnt(0)
	v_mfma_f32_32x32x16_f16 v[80:95], v[176:179], v[144:147], v[112:127]
	ds_read_b128 v[176:179], v225 offset:0
	s_waitcnt vmcnt(3)
	v_exp_f32_e32 v64, v64
	v_exp_f32_e32 v65, v65
	v_cvt_pk_f16_f32 v216, v216, v217
	v_cvt_pk_f16_f32 v217, v218, v219
	v_cvt_pk_f16_f32 v218, v220, v221
	v_cvt_pk_f16_f32 v219, v222, v223
	v_mfma_f32_32x32x16_f16 v[80:95], v[180:183], v[148:151], v[80:95]
	ds_write_b128 v228, v[216:219] offset:0
	ds_read_b128 v[180:183], v225 offset:32
	v_cvt_pk_f16_f32 v160, v64, v65
	v_add_f32_e32 v64, v64, v65
	v_exp_f32_e32 v66, v66
	v_exp_f32_e32 v67, v67
	v_mfma_f32_32x32x16_f16 v[80:95], v[184:187], v[152:155], v[80:95]
	ds_read_b128 v[184:187], v225 offset:64
	v_cvt_pk_f16_f32 v161, v66, v67
	v_add_f32_e32 v66, v66, v67
	v_exp_f32_e32 v68, v68
	v_exp_f32_e32 v69, v69
	v_mfma_f32_32x32x16_f16 v[80:95], v[188:191], v[156:159], v[80:95]
	ds_read_b128 v[188:191], v225 offset:96
	v_cvt_pk_f16_f32 v162, v68, v69
	v_add_f32_e32 v68, v68, v69
	v_add_f32_e32 v231, v64, v66
	v_exp_f32_e32 v70, v70
	v_exp_f32_e32 v71, v71
	v_mfma_f32_32x32x16_f16 v[32:47], v[192:195], v[168:171], v[32:47]
	ds_read_b128 v[192:195], v226 offset:27712
	v_cvt_pk_f16_f32 v163, v70, v71
	v_add_f32_e32 v70, v70, v71
	v_add_f32_e32 v231, v231, v68
	v_exp_f32_e32 v72, v72
	v_exp_f32_e32 v73, v73
	v_mfma_f32_32x32x16_f16 v[48:63], v[196:199], v[168:171], v[48:63]
	ds_read_b128 v[196:199], v226 offset:32320
	v_cvt_pk_f16_f32 v164, v72, v73
	v_add_f32_e32 v72, v72, v73
	v_add_f32_e32 v231, v231, v70
	v_exp_f32_e32 v74, v74
	v_exp_f32_e32 v75, v75
	v_mfma_f32_32x32x16_f16 v[32:47], v[200:203], v[172:175], v[32:47]
	ds_read_b128 v[200:203], v226 offset:27744
	v_cvt_pk_f16_f32 v165, v74, v75
	v_add_f32_e32 v74, v74, v75
	v_add_f32_e32 v231, v231, v72
	v_exp_f32_e32 v76, v76
	v_exp_f32_e32 v77, v77
	v_mfma_f32_32x32x16_f16 v[48:63], v[204:207], v[172:175], v[48:63]
	ds_read_b128 v[204:207], v226 offset:32352
	v_cvt_pk_f16_f32 v166, v76, v77
	v_add_f32_e32 v76, v76, v77
	v_add_f32_e32 v231, v231, v74
	v_exp_f32_e32 v78, v78
	v_exp_f32_e32 v79, v79
	v_add_f32_e32 v231, v231, v76
	v_cvt_pk_f16_f32 v167, v78, v79
	v_add_f32_e32 v78, v78, v79
	v_add_f32_e32 v231, v231, v78
	v_cmp_nge_f32_e32 vcc, s34, v231
	s_cbranch_vccnz .Lovf_a31

.Lovfret_b31:
	v_add_f32_e32 v233, v233, v231
	s_waitcnt lgkmcnt(7)
	s_barrier
	s_add_u32 s23, s23, 1
	s_add_u32 s27, s27, 1
	s_cmp_eq_u32 s27, 7
	s_cbranch_scc0 .Lbody
	s_nop 15
	s_nop 7
	v_mov_b32_e32 v235, v232
	v_mov_b32_e32 v236, v232
	s_nop 1
	v_permlane32_swap_b32_e32 v235, v236
	v_add_f32_e32 v236, v235, v236
	v_rcp_f32_e32 v237, v236
	s_nop 0
	v_fma_f32 v238, -v236, v237, 1.0
	v_fmac_f32_e32 v237, v238, v237
	v_mul_f32_e32 v0, v237, v0
	v_mul_f32_e32 v1, v237, v1
	v_mul_f32_e32 v2, v237, v2
	v_mul_f32_e32 v3, v237, v3
	v_mul_f32_e32 v4, v237, v4
	v_mul_f32_e32 v5, v237, v5
	v_mul_f32_e32 v6, v237, v6
	v_mul_f32_e32 v7, v237, v7
	v_mul_f32_e32 v8, v237, v8
	v_mul_f32_e32 v9, v237, v9
	v_mul_f32_e32 v10, v237, v10
	v_mul_f32_e32 v11, v237, v11
	v_mul_f32_e32 v12, v237, v12
	v_mul_f32_e32 v13, v237, v13
	v_mul_f32_e32 v14, v237, v14
	v_mul_f32_e32 v15, v237, v15
	v_mul_f32_e32 v16, v237, v16
	v_mul_f32_e32 v17, v237, v17
	v_mul_f32_e32 v18, v237, v18
	v_mul_f32_e32 v19, v237, v19
	v_mul_f32_e32 v20, v237, v20
	v_mul_f32_e32 v21, v237, v21
	v_mul_f32_e32 v22, v237, v22
	v_mul_f32_e32 v23, v237, v23
	v_mul_f32_e32 v24, v237, v24
	v_mul_f32_e32 v25, v237, v25
	v_mul_f32_e32 v26, v237, v26
	v_mul_f32_e32 v27, v237, v27
	v_mul_f32_e32 v28, v237, v28
	v_mul_f32_e32 v29, v237, v29
	v_mul_f32_e32 v30, v237, v30
	v_mul_f32_e32 v31, v237, v31
	ds_write_b128 v241, v[0:3] offset:0
	ds_write_b128 v241, v[16:19] offset:128
	ds_write_b128 v241, v[4:7] offset:32
	ds_write_b128 v241, v[20:23] offset:160
	ds_write_b128 v241, v[8:11] offset:64
	ds_write_b128 v241, v[24:27] offset:192
	ds_write_b128 v241, v[12:15] offset:96
	ds_write_b128 v241, v[28:31] offset:224
	s_waitcnt lgkmcnt(0)
	ds_read_b128 v[0:3], v242 offset:0
	ds_read_b128 v[4:7], v242 offset:1088
	ds_read_b128 v[8:11], v242 offset:2176
	ds_read_b128 v[12:15], v242 offset:3264
	ds_read_b128 v[16:19], v242 offset:4352
	ds_read_b128 v[20:23], v242 offset:5440
	ds_read_b128 v[24:27], v242 offset:6528
	ds_read_b128 v[28:31], v242 offset:7616
	s_waitcnt lgkmcnt(7)
	s_add_u32 s31, s30, 0x0
	buffer_store_dwordx4 v[0:3], v244, s[12:15], s31 offen nt sc1
	s_waitcnt lgkmcnt(6)
	s_add_u32 s31, s30, 0x4000
	buffer_store_dwordx4 v[4:7], v244, s[12:15], s31 offen nt sc1
	s_waitcnt lgkmcnt(5)
	s_add_u32 s31, s30, 0x8000
	buffer_store_dwordx4 v[8:11], v244, s[12:15], s31 offen nt sc1
	s_waitcnt lgkmcnt(4)
	s_add_u32 s31, s30, 0xc000
	buffer_store_dwordx4 v[12:15], v244, s[12:15], s31 offen nt sc1
	s_waitcnt lgkmcnt(3)
	s_add_u32 s31, s30, 0x10000
	buffer_store_dwordx4 v[16:19], v244, s[12:15], s31 offen nt sc1
	s_waitcnt lgkmcnt(2)
	s_add_u32 s31, s30, 0x14000
	buffer_store_dwordx4 v[20:23], v244, s[12:15], s31 offen nt sc1
	s_waitcnt lgkmcnt(1)
	s_add_u32 s31, s30, 0x18000
	buffer_store_dwordx4 v[24:27], v244, s[12:15], s31 offen nt sc1
	s_waitcnt lgkmcnt(0)
	s_add_u32 s31, s30, 0x1c000
	buffer_store_dwordx4 v[28:31], v244, s[12:15], s31 offen nt sc1
	s_nop 1
	s_waitcnt lgkmcnt(0)
	v_mfma_f32_32x32x16_f16 v[80:95], v[176:179], v[144:147], v[112:127]
	ds_read_b128 v[176:179], v225 offset:4608
	v_mfma_f32_32x32x16_f16 v[80:95], v[180:183], v[148:151], v[80:95]
	ds_read_b128 v[180:183], v225 offset:4640
	v_mfma_f32_32x32x16_f16 v[80:95], v[184:187], v[152:155], v[80:95]
	ds_read_b128 v[184:187], v225 offset:4672
	v_mfma_f32_32x32x16_f16 v[80:95], v[188:191], v[156:159], v[80:95]
	ds_read_b128 v[188:191], v225 offset:4704
	s_nop 15
	s_nop 3
	s_waitcnt vmcnt(8)
	v_cmp_ne_u32_e64 s[20:21], 0, v224
	s_add_u32 s31, s23, 1
	s_and_b32 s31, s31, 31
	s_lshl_b32 s31, s31, 8
	s_add_u32 s26, s31, s22
	s_add_u32 s31, s23, 3
	s_and_b32 s31, s31, 31
	s_mul_i32 s31, s31, 0xc0000
	s_add_u32 s24, s31, s18
	s_add_u32 s31, s23, 2
	s_and_b32 s31, s31, 31
	s_mul_i32 s31, s31, 0xc0000
	s_add_u32 s25, s31, s19
	s_cmp_eq_u64 s[20:21], -1
	s_cselect_b32 s34, s37, s38
	s_waitcnt lgkmcnt(0)
	v_mfma_f32_32x32x16_f16 v[64:79], v[176:179], v[144:147], v[112:127]
	ds_read_b128 v[176:179], v225 offset:9216
	buffer_load_dword v224, v230, s[8:11], s26 offen
	v_exp_f32_e32 v80, v80
	v_exp_f32_e32 v81, v81
	v_cvt_pk_f16_f32 v208, v208, v209
	v_cvt_pk_f16_f32 v209, v210, v211
	v_cvt_pk_f16_f32 v212, v212, v213
	v_cvt_pk_f16_f32 v213, v214, v215
	v_mfma_f32_32x32x16_f16 v[64:79], v[180:183], v[148:151], v[64:79]
	ds_write_b64 v227, v[208:209] offset:18432
	ds_write_b64 v227, v[212:213] offset:23040
	ds_read_b128 v[180:183], v225 offset:9248
	v_cvt_pk_f16_f32 v160, v80, v81
	v_add_f32_e32 v80, v80, v81
	v_exp_f32_e32 v82, v82
	v_exp_f32_e32 v83, v83
	v_mfma_f32_32x32x16_f16 v[64:79], v[184:187], v[152:155], v[64:79]
	ds_read_b128 v[184:187], v225 offset:9280
	v_cvt_pk_f16_f32 v161, v82, v83
	v_add_f32_e32 v82, v82, v83
	v_exp_f32_e32 v84, v84
	v_exp_f32_e32 v85, v85
	v_mfma_f32_32x32x16_f16 v[64:79], v[188:191], v[156:159], v[64:79]
	ds_read_b128 v[188:191], v225 offset:9312
	buffer_load_dwordx4 v[208:211], v229, s[4:7], s24 offen
	v_cvt_pk_f16_f32 v162, v84, v85
	v_add_f32_e32 v84, v84, v85
	v_add_f32_e32 v231, v80, v82
	v_exp_f32_e32 v86, v86
	v_exp_f32_e32 v87, v87
	s_waitcnt lgkmcnt(10)
	v_mfma_f32_32x32x16_f16 v[32:47], v[192:195], v[168:171], v[32:47]
	ds_read_b128 v[192:195], v226 offset:0
	buffer_load_dwordx4 v[212:215], v252, s[4:7], s24 offen
	v_cvt_pk_f16_f32 v163, v86, v87
	v_add_f32_e32 v86, v86, v87
	v_add_f32_e32 v231, v231, v84
	v_exp_f32_e32 v88, v88
	v_exp_f32_e32 v89, v89
	v_mfma_f32_32x32x16_f16 v[48:63], v[196:199], v[168:171], v[48:63]
	ds_read_b128 v[196:199], v226 offset:4608
	v_cvt_pk_f16_f32 v164, v88, v89
	v_add_f32_e32 v88, v88, v89
	v_add_f32_e32 v231, v231, v86
	v_exp_f32_e32 v90, v90
	v_exp_f32_e32 v91, v91
	v_mfma_f32_32x32x16_f16 v[32:47], v[200:203], v[172:175], v[32:47]
	ds_read_b128 v[200:203], v226 offset:32
	v_cvt_pk_f16_f32 v165, v90, v91
	v_add_f32_e32 v90, v90, v91
	v_add_f32_e32 v231, v231, v88
	v_exp_f32_e32 v92, v92
	v_exp_f32_e32 v93, v93
	v_mfma_f32_32x32x16_f16 v[48:63], v[204:207], v[172:175], v[48:63]
	ds_read_b128 v[204:207], v226 offset:4640
	v_cvt_pk_f16_f32 v166, v92, v93
	v_add_f32_e32 v92, v92, v93
	v_add_f32_e32 v231, v231, v90
	v_exp_f32_e32 v94, v94
	v_exp_f32_e32 v95, v95
	v_add_f32_e32 v231, v231, v92
	v_cvt_pk_f16_f32 v167, v94, v95
	v_add_f32_e32 v94, v94, v95
	v_add_f32_e32 v231, v231, v94
	v_cmp_nge_f32_e32 vcc, s34, v231
	s_cbranch_vccnz .Lovf_b1_00
.Lovfret_b1_00:
	v_add_f32_e32 v233, v233, v231
	s_waitcnt lgkmcnt(4)
	v_mfma_f32_32x32x16_f16 v[80:95], v[176:179], v[144:147], v[112:127]
	ds_read_b128 v[176:179], v225 offset:13824
	s_waitcnt vmcnt(3)
	v_exp_f32_e32 v64, v64
	v_exp_f32_e32 v65, v65
	v_cvt_pk_f16_f32 v216, v216, v217
	v_cvt_pk_f16_f32 v217, v218, v219
	v_cvt_pk_f16_f32 v218, v220, v221
	v_cvt_pk_f16_f32 v219, v222, v223
	v_mfma_f32_32x32x16_f16 v[80:95], v[180:183], v[148:151], v[80:95]
	ds_write_b128 v228, v[216:219] offset:9216
	ds_read_b128 v[180:183], v225 offset:13856
	v_cvt_pk_f16_f32 v168, v64, v65
	v_add_f32_e32 v64, v64, v65
	v_exp_f32_e32 v66, v66
	v_exp_f32_e32 v67, v67
	v_mfma_f32_32x32x16_f16 v[80:95], v[184:187], v[152:155], v[80:95]
	ds_read_b128 v[184:187], v225 offset:13888
	v_cvt_pk_f16_f32 v169, v66, v67
	v_add_f32_e32 v66, v66, v67
	v_exp_f32_e32 v68, v68
	v_exp_f32_e32 v69, v69
	v_mfma_f32_32x32x16_f16 v[80:95], v[188:191], v[156:159], v[80:95]
	ds_read_b128 v[188:191], v225 offset:13920
	buffer_load_dword v216, v230, s[4:7], s25 offen
	buffer_load_dword v217, v245, s[4:7], s25 offen
	v_cvt_pk_f16_f32 v170, v68, v69
	v_add_f32_e32 v68, v68, v69
	v_add_f32_e32 v231, v64, v66
	v_exp_f32_e32 v70, v70
	v_exp_f32_e32 v71, v71
	s_waitcnt lgkmcnt(5)
	v_mfma_f32_32x32x16_f16 v[32:47], v[192:195], v[160:163], v[32:47]
	ds_read_b128 v[192:195], v226 offset:64
	buffer_load_dword v218, v246, s[4:7], s25 offen
	buffer_load_dword v219, v247, s[4:7], s25 offen
	v_cvt_pk_f16_f32 v171, v70, v71
	v_add_f32_e32 v70, v70, v71
	v_add_f32_e32 v231, v231, v68
	v_exp_f32_e32 v72, v72
	v_exp_f32_e32 v73, v73
	v_mfma_f32_32x32x16_f16 v[48:63], v[196:199], v[160:163], v[48:63]
	ds_read_b128 v[196:199], v226 offset:4672
	buffer_load_dword v220, v248, s[4:7], s25 offen
	buffer_load_dword v221, v249, s[4:7], s25 offen
	v_cvt_pk_f16_f32 v172, v72, v73
	v_add_f32_e32 v72, v72, v73
	v_add_f32_e32 v231, v231, v70
	v_exp_f32_e32 v74, v74
	v_exp_f32_e32 v75, v75
	v_mfma_f32_32x32x16_f16 v[32:47], v[200:203], v[164:167], v[32:47]
	ds_read_b128 v[200:203], v226 offset:96
	buffer_load_dword v222, v250, s[4:7], s25 offen
	v_cvt_pk_f16_f32 v173, v74, v75
	v_add_f32_e32 v74, v74, v75
	v_add_f32_e32 v231, v231, v72
	v_exp_f32_e32 v76, v76
	v_exp_f32_e32 v77, v77
	v_mfma_f32_32x32x16_f16 v[48:63], v[204:207], v[164:167], v[48:63]
	ds_read_b128 v[204:207], v226 offset:4704
	buffer_load_dword v223, v251, s[4:7], s25 offen
	v_cvt_pk_f16_f32 v174, v76, v77
	v_add_f32_e32 v76, v76, v77
	v_add_f32_e32 v231, v231, v74
	v_exp_f32_e32 v78, v78
	v_exp_f32_e32 v79, v79
	v_add_f32_e32 v231, v231, v76
	v_cvt_pk_f16_f32 v175, v78, v79
	v_add_f32_e32 v78, v78, v79
	v_add_f32_e32 v231, v231, v78
	v_cmp_nge_f32_e32 vcc, s34, v231
	s_cbranch_vccnz .Lovf_b1_01
.Lovfret_b1_01:
	v_add_f32_e32 v233, v233, v231
	s_waitcnt lgkmcnt(7)
	s_barrier
	s_add_u32 s23, s23, 1
	s_waitcnt vmcnt(8)
	v_cmp_ne_u32_e64 s[20:21], 0, v224
	s_add_u32 s31, s23, 1
	s_and_b32 s31, s31, 31
	s_lshl_b32 s31, s31, 8
	s_add_u32 s26, s31, s22
	s_add_u32 s31, s23, 3
	s_and_b32 s31, s31, 31
	s_mul_i32 s31, s31, 0xc0000
	s_add_u32 s24, s31, s18
	s_add_u32 s31, s23, 2
	s_and_b32 s31, s31, 31
	s_mul_i32 s31, s31, 0xc0000
	s_add_u32 s25, s31, s19
	s_cmp_eq_u64 s[20:21], -1
	s_cselect_b32 s34, s37, s38
	s_waitcnt lgkmcnt(4)
	v_mfma_f32_32x32x16_f16 v[64:79], v[176:179], v[144:147], v[112:127]
	ds_read_b128 v[176:179], v225 offset:18432
	buffer_load_dword v224, v230, s[8:11], s26 offen
	v_exp_f32_e32 v80, v80
	v_exp_f32_e32 v81, v81
	v_cvt_pk_f16_f32 v208, v208, v209
	v_cvt_pk_f16_f32 v209, v210, v211
	v_cvt_pk_f16_f32 v212, v212, v213
	v_cvt_pk_f16_f32 v213, v214, v215
	v_mfma_f32_32x32x16_f16 v[64:79], v[180:183], v[148:151], v[64:79]
	ds_write_b64 v227, v[208:209] offset:27648
	ds_write_b64 v227, v[212:213] offset:32256
	ds_read_b128 v[180:183], v225 offset:18464
	v_cvt_pk_f16_f32 v160, v80, v81
	v_add_f32_e32 v80, v80, v81
	v_exp_f32_e32 v82, v82
	v_exp_f32_e32 v83, v83
	v_mfma_f32_32x32x16_f16 v[64:79], v[184:187], v[152:155], v[64:79]
	ds_read_b128 v[184:187], v225 offset:18496
	v_cvt_pk_f16_f32 v161, v82, v83
	v_add_f32_e32 v82, v82, v83
	v_exp_f32_e32 v84, v84
	v_exp_f32_e32 v85, v85
	v_mfma_f32_32x32x16_f16 v[64:79], v[188:191], v[156:159], v[64:79]
	ds_read_b128 v[188:191], v225 offset:18528
	buffer_load_dwordx4 v[208:211], v229, s[4:7], s24 offen
	v_cvt_pk_f16_f32 v162, v84, v85
	v_add_f32_e32 v84, v84, v85
	v_add_f32_e32 v231, v80, v82
	v_exp_f32_e32 v86, v86
	v_exp_f32_e32 v87, v87
	s_waitcnt lgkmcnt(6)
	v_mfma_f32_32x32x16_f16 v[32:47], v[192:195], v[168:171], v[32:47]
	ds_read_b128 v[192:195], v226 offset:9216
	buffer_load_dwordx4 v[212:215], v252, s[4:7], s24 offen
	v_cvt_pk_f16_f32 v163, v86, v87
	v_add_f32_e32 v86, v86, v87
	v_add_f32_e32 v231, v231, v84
	v_exp_f32_e32 v88, v88
	v_exp_f32_e32 v89, v89
	v_mfma_f32_32x32x16_f16 v[48:63], v[196:199], v[168:171], v[48:63]
	ds_read_b128 v[196:199], v226 offset:13824
	v_cvt_pk_f16_f32 v164, v88, v89
	v_add_f32_e32 v88, v88, v89
	v_add_f32_e32 v231, v231, v86
	v_exp_f32_e32 v90, v90
	v_exp_f32_e32 v91, v91
	v_mfma_f32_32x32x16_f16 v[32:47], v[200:203], v[172:175], v[32:47]
	ds_read_b128 v[200:203], v226 offset:9248
	v_cvt_pk_f16_f32 v165, v90, v91
	v_add_f32_e32 v90, v90, v91
	v_add_f32_e32 v231, v231, v88
	v_exp_f32_e32 v92, v92
	v_exp_f32_e32 v93, v93
	v_mfma_f32_32x32x16_f16 v[48:63], v[204:207], v[172:175], v[48:63]
	ds_read_b128 v[204:207], v226 offset:13856
	v_cvt_pk_f16_f32 v166, v92, v93
	v_add_f32_e32 v92, v92, v93
	v_add_f32_e32 v231, v231, v90
	v_exp_f32_e32 v94, v94
	v_exp_f32_e32 v95, v95
	v_add_f32_e32 v231, v231, v92
	v_cvt_pk_f16_f32 v167, v94, v95
	v_add_f32_e32 v94, v94, v95
	v_add_f32_e32 v231, v231, v94
	v_cmp_nge_f32_e32 vcc, s34, v231
	s_cbranch_vccnz .Lovf_b1_10
.Lovfret_b1_10:
	v_add_f32_e32 v233, v233, v231
	s_waitcnt lgkmcnt(4)
	v_mfma_f32_32x32x16_f16 v[80:95], v[176:179], v[144:147], v[112:127]
	ds_read_b128 v[176:179], v225 offset:23040
	s_waitcnt vmcnt(3)
	v_exp_f32_e32 v64, v64
	v_exp_f32_e32 v65, v65
	v_cvt_pk_f16_f32 v216, v216, v217
	v_cvt_pk_f16_f32 v217, v218, v219
	v_cvt_pk_f16_f32 v218, v220, v221
	v_cvt_pk_f16_f32 v219, v222, v223
	v_mfma_f32_32x32x16_f16 v[80:95], v[180:183], v[148:151], v[80:95]
	ds_write_b128 v228, v[216:219] offset:18432
	ds_read_b128 v[180:183], v225 offset:23072
	v_cvt_pk_f16_f32 v168, v64, v65
	v_add_f32_e32 v64, v64, v65
	v_exp_f32_e32 v66, v66
	v_exp_f32_e32 v67, v67
	v_mfma_f32_32x32x16_f16 v[80:95], v[184:187], v[152:155], v[80:95]
	ds_read_b128 v[184:187], v225 offset:23104
	v_cvt_pk_f16_f32 v169, v66, v67
	v_add_f32_e32 v66, v66, v67
	v_exp_f32_e32 v68, v68
	v_exp_f32_e32 v69, v69
	v_mfma_f32_32x32x16_f16 v[80:95], v[188:191], v[156:159], v[80:95]
	ds_read_b128 v[188:191], v225 offset:23136
	buffer_load_dword v216, v230, s[4:7], s25 offen
	buffer_load_dword v217, v245, s[4:7], s25 offen
	v_cvt_pk_f16_f32 v170, v68, v69
	v_add_f32_e32 v68, v68, v69
	v_add_f32_e32 v231, v64, v66
	v_exp_f32_e32 v70, v70
	v_exp_f32_e32 v71, v71
	s_waitcnt lgkmcnt(5)
	v_mfma_f32_32x32x16_f16 v[32:47], v[192:195], v[160:163], v[32:47]
	ds_read_b128 v[192:195], v226 offset:9280
	buffer_load_dword v218, v246, s[4:7], s25 offen
	buffer_load_dword v219, v247, s[4:7], s25 offen
	v_cvt_pk_f16_f32 v171, v70, v71
	v_add_f32_e32 v70, v70, v71
	v_add_f32_e32 v231, v231, v68
	v_exp_f32_e32 v72, v72
	v_exp_f32_e32 v73, v73
	v_mfma_f32_32x32x16_f16 v[48:63], v[196:199], v[160:163], v[48:63]
	ds_read_b128 v[196:199], v226 offset:13888
	buffer_load_dword v220, v248, s[4:7], s25 offen
	buffer_load_dword v221, v249, s[4:7], s25 offen
	v_cvt_pk_f16_f32 v172, v72, v73
	v_add_f32_e32 v72, v72, v73
	v_add_f32_e32 v231, v231, v70
	v_exp_f32_e32 v74, v74
	v_exp_f32_e32 v75, v75
	v_mfma_f32_32x32x16_f16 v[32:47], v[200:203], v[164:167], v[32:47]
	ds_read_b128 v[200:203], v226 offset:9312
	buffer_load_dword v222, v250, s[4:7], s25 offen
	v_cvt_pk_f16_f32 v173, v74, v75
	v_add_f32_e32 v74, v74, v75
	v_add_f32_e32 v231, v231, v72
	v_exp_f32_e32 v76, v76
	v_exp_f32_e32 v77, v77
	v_mfma_f32_32x32x16_f16 v[48:63], v[204:207], v[164:167], v[48:63]
	ds_read_b128 v[204:207], v226 offset:13920
	buffer_load_dword v223, v251, s[4:7], s25 offen
	v_cvt_pk_f16_f32 v174, v76, v77
	v_add_f32_e32 v76, v76, v77
	v_add_f32_e32 v231, v231, v74
	v_exp_f32_e32 v78, v78
	v_exp_f32_e32 v79, v79
	v_add_f32_e32 v231, v231, v76
	v_cvt_pk_f16_f32 v175, v78, v79
	v_add_f32_e32 v78, v78, v79
	v_add_f32_e32 v231, v231, v78
	v_cmp_nge_f32_e32 vcc, s34, v231
	s_cbranch_vccnz .Lovf_b1_11
.Lovfret_b1_11:
	v_add_f32_e32 v233, v233, v231
	s_waitcnt lgkmcnt(7)
	s_barrier
	s_add_u32 s23, s23, 1
	s_waitcnt vmcnt(8)
	v_cmp_ne_u32_e64 s[20:21], 0, v224
	s_add_u32 s31, s23, 1
	s_and_b32 s31, s31, 31
	s_lshl_b32 s31, s31, 8
	s_add_u32 s26, s31, s22
	s_add_u32 s31, s23, 3
	s_and_b32 s31, s31, 31
	s_mul_i32 s31, s31, 0xc0000
	s_add_u32 s24, s31, s18
	s_add_u32 s31, s23, 2
	s_and_b32 s31, s31, 31
	s_mul_i32 s31, s31, 0xc0000
	s_add_u32 s25, s31, s19
	s_cmp_eq_u64 s[20:21], -1
	s_cselect_b32 s34, s37, s38
	s_waitcnt lgkmcnt(4)
	v_mfma_f32_32x32x16_f16 v[64:79], v[176:179], v[144:147], v[112:127]
	ds_read_b128 v[176:179], v225 offset:27648
	buffer_load_dword v224, v230, s[8:11], s26 offen
	v_exp_f32_e32 v80, v80
	v_exp_f32_e32 v81, v81
	v_cvt_pk_f16_f32 v208, v208, v209
	v_cvt_pk_f16_f32 v209, v210, v211
	v_cvt_pk_f16_f32 v212, v212, v213
	v_cvt_pk_f16_f32 v213, v214, v215
	v_mfma_f32_32x32x16_f16 v[64:79], v[180:183], v[148:151], v[64:79]
	ds_write_b64 v227, v[208:209] offset:0
	ds_write_b64 v227, v[212:213] offset:4608
	ds_read_b128 v[180:183], v225 offset:27680
	v_cvt_pk_f16_f32 v160, v80, v81
	v_add_f32_e32 v80, v80, v81
	v_exp_f32_e32 v82, v82
	v_exp_f32_e32 v83, v83
	v_mfma_f32_32x32x16_f16 v[64:79], v[184:187], v[152:155], v[64:79]
	ds_read_b128 v[184:187], v225 offset:27712
	v_cvt_pk_f16_f32 v161, v82, v83
	v_add_f32_e32 v82, v82, v83
	v_exp_f32_e32 v84, v84
	v_exp_f32_e32 v85, v85
	v_mfma_f32_32x32x16_f16 v[64:79], v[188:191], v[156:159], v[64:79]
	ds_read_b128 v[188:191], v225 offset:27744
	buffer_load_dwordx4 v[208:211], v229, s[4:7], s24 offen
	v_cvt_pk_f16_f32 v162, v84, v85
	v_add_f32_e32 v84, v84, v85
	v_add_f32_e32 v231, v80, v82
	v_exp_f32_e32 v86, v86
	v_exp_f32_e32 v87, v87
	s_waitcnt lgkmcnt(6)
	v_mfma_f32_32x32x16_f16 v[32:47], v[192:195], v[168:171], v[32:47]
	ds_read_b128 v[192:195], v226 offset:18432
	buffer_load_dwordx4 v[212:215], v252, s[4:7], s24 offen
	v_cvt_pk_f16_f32 v163, v86, v87
	v_add_f32_e32 v86, v86, v87
	v_add_f32_e32 v231, v231, v84
	v_exp_f32_e32 v88, v88
	v_exp_f32_e32 v89, v89
	v_mfma_f32_32x32x16_f16 v[48:63], v[196:199], v[168:171], v[48:63]
	ds_read_b128 v[196:199], v226 offset:23040
	v_cvt_pk_f16_f32 v164, v88, v89
	v_add_f32_e32 v88, v88, v89
	v_add_f32_e32 v231, v231, v86
	v_exp_f32_e32 v90, v90
	v_exp_f32_e32 v91, v91
	v_mfma_f32_32x32x16_f16 v[32:47], v[200:203], v[172:175], v[32:47]
	ds_read_b128 v[200:203], v226 offset:18464
	v_cvt_pk_f16_f32 v165, v90, v91
	v_add_f32_e32 v90, v90, v91
	v_add_f32_e32 v231, v231, v88
	v_exp_f32_e32 v92, v92
	v_exp_f32_e32 v93, v93
	v_mfma_f32_32x32x16_f16 v[48:63], v[204:207], v[172:175], v[48:63]
	ds_read_b128 v[204:207], v226 offset:23072
	v_cvt_pk_f16_f32 v166, v92, v93
	v_add_f32_e32 v92, v92, v93
	v_add_f32_e32 v231, v231, v90
	v_exp_f32_e32 v94, v94
	v_exp_f32_e32 v95, v95
	v_add_f32_e32 v231, v231, v92
	v_cvt_pk_f16_f32 v167, v94, v95
	v_add_f32_e32 v94, v94, v95
	v_add_f32_e32 v231, v231, v94
	v_cmp_nge_f32_e32 vcc, s34, v231
	s_cbranch_vccnz .Lovf_b1_20
.Lovfret_b1_20:
	v_add_f32_e32 v233, v233, v231
	s_waitcnt lgkmcnt(4)
	v_mfma_f32_32x32x16_f16 v[80:95], v[176:179], v[144:147], v[112:127]
	ds_read_b128 v[176:179], v225 offset:32256
	s_waitcnt vmcnt(3)
	v_exp_f32_e32 v64, v64
	v_exp_f32_e32 v65, v65
	v_cvt_pk_f16_f32 v216, v216, v217
	v_cvt_pk_f16_f32 v217, v218, v219
	v_cvt_pk_f16_f32 v218, v220, v221
	v_cvt_pk_f16_f32 v219, v222, v223
	v_mfma_f32_32x32x16_f16 v[80:95], v[180:183], v[148:151], v[80:95]
	ds_write_b128 v228, v[216:219] offset:27648
	ds_read_b128 v[180:183], v225 offset:32288
	v_cvt_pk_f16_f32 v168, v64, v65
	v_add_f32_e32 v64, v64, v65
	v_exp_f32_e32 v66, v66
	v_exp_f32_e32 v67, v67
	v_mfma_f32_32x32x16_f16 v[80:95], v[184:187], v[152:155], v[80:95]
	ds_read_b128 v[184:187], v225 offset:32320
	v_cvt_pk_f16_f32 v169, v66, v67
	v_add_f32_e32 v66, v66, v67
	v_exp_f32_e32 v68, v68
	v_exp_f32_e32 v69, v69
	v_mfma_f32_32x32x16_f16 v[80:95], v[188:191], v[156:159], v[80:95]
	ds_read_b128 v[188:191], v225 offset:32352
	buffer_load_dword v216, v230, s[4:7], s25 offen
	buffer_load_dword v217, v245, s[4:7], s25 offen
	v_cvt_pk_f16_f32 v170, v68, v69
	v_add_f32_e32 v68, v68, v69
	v_add_f32_e32 v231, v64, v66
	v_exp_f32_e32 v70, v70
	v_exp_f32_e32 v71, v71
	s_waitcnt lgkmcnt(5)
	v_mfma_f32_32x32x16_f16 v[32:47], v[192:195], v[160:163], v[32:47]
	ds_read_b128 v[192:195], v226 offset:18496
	buffer_load_dword v218, v246, s[4:7], s25 offen
	buffer_load_dword v219, v247, s[4:7], s25 offen
	v_cvt_pk_f16_f32 v171, v70, v71
	v_add_f32_e32 v70, v70, v71
	v_add_f32_e32 v231, v231, v68
	v_exp_f32_e32 v72, v72
	v_exp_f32_e32 v73, v73
	v_mfma_f32_32x32x16_f16 v[48:63], v[196:199], v[160:163], v[48:63]
	ds_read_b128 v[196:199], v226 offset:23104
	buffer_load_dword v220, v248, s[4:7], s25 offen
	buffer_load_dword v221, v249, s[4:7], s25 offen
	v_cvt_pk_f16_f32 v172, v72, v73
	v_add_f32_e32 v72, v72, v73
	v_add_f32_e32 v231, v231, v70
	v_exp_f32_e32 v74, v74
	v_exp_f32_e32 v75, v75
	v_mfma_f32_32x32x16_f16 v[32:47], v[200:203], v[164:167], v[32:47]
	ds_read_b128 v[200:203], v226 offset:18528
	buffer_load_dword v222, v250, s[4:7], s25 offen
	v_cvt_pk_f16_f32 v173, v74, v75
	v_add_f32_e32 v74, v74, v75
	v_add_f32_e32 v231, v231, v72
	v_exp_f32_e32 v76, v76
	v_exp_f32_e32 v77, v77
	v_mfma_f32_32x32x16_f16 v[48:63], v[204:207], v[164:167], v[48:63]
	ds_read_b128 v[204:207], v226 offset:23136
	buffer_load_dword v223, v251, s[4:7], s25 offen
	v_cvt_pk_f16_f32 v174, v76, v77
	v_add_f32_e32 v76, v76, v77
	v_add_f32_e32 v231, v231, v74
	v_exp_f32_e32 v78, v78
	v_exp_f32_e32 v79, v79
	v_add_f32_e32 v231, v231, v76
	v_cvt_pk_f16_f32 v175, v78, v79
	v_add_f32_e32 v78, v78, v79
	v_add_f32_e32 v231, v231, v78
	v_cmp_nge_f32_e32 vcc, s34, v231
	s_cbranch_vccnz .Lovf_b1_21
.Lovfret_b1_21:
	v_add_f32_e32 v233, v233, v231
	s_waitcnt lgkmcnt(7)
	s_barrier
	s_add_u32 s23, s23, 1
	s_waitcnt vmcnt(8)
	v_cmp_ne_u32_e64 s[20:21], 0, v224
	s_add_u32 s31, s23, 1
	s_and_b32 s31, s31, 31
	s_lshl_b32 s31, s31, 8
	s_add_u32 s26, s31, s22
	s_add_u32 s31, s23, 3
	s_and_b32 s31, s31, 31
	s_mul_i32 s31, s31, 0xc0000
	s_add_u32 s24, s31, s18
	s_add_u32 s31, s23, 2
	s_and_b32 s31, s31, 31
	s_mul_i32 s31, s31, 0xc0000
	s_add_u32 s25, s31, s19
	s_cmp_eq_u64 s[20:21], -1
	s_cselect_b32 s34, s37, s38
	s_waitcnt lgkmcnt(4)
	v_mfma_f32_32x32x16_f16 v[64:79], v[176:179], v[144:147], v[112:127]
	ds_read_b128 v[176:179], v225 offset:0
	buffer_load_dword v224, v230, s[8:11], s26 offen
	v_exp_f32_e32 v80, v80
	v_exp_f32_e32 v81, v81
	v_cvt_pk_f16_f32 v208, v208, v209
	v_cvt_pk_f16_f32 v209, v210, v211
	v_cvt_pk_f16_f32 v212, v212, v213
	v_cvt_pk_f16_f32 v213, v214, v215
	v_mfma_f32_32x32x16_f16 v[64:79], v[180:183], v[148:151], v[64:79]
	ds_write_b64 v227, v[208:209] offset:9216
	ds_write_b64 v227, v[212:213] offset:13824
	ds_read_b128 v[180:183], v225 offset:32
	v_cvt_pk_f16_f32 v160, v80, v81
	v_add_f32_e32 v80, v80, v81
	v_exp_f32_e32 v82, v82
	v_exp_f32_e32 v83, v83
	v_mfma_f32_32x32x16_f16 v[64:79], v[184:187], v[152:155], v[64:79]
	ds_read_b128 v[184:187], v225 offset:64
	v_cvt_pk_f16_f32 v161, v82, v83
	v_add_f32_e32 v82, v82, v83
	v_exp_f32_e32 v84, v84
	v_exp_f32_e32 v85, v85
	v_mfma_f32_32x32x16_f16 v[64:79], v[188:191], v[156:159], v[64:79]
	ds_read_b128 v[188:191], v225 offset:96
	buffer_load_dwordx4 v[208:211], v229, s[4:7], s24 offen
	v_cvt_pk_f16_f32 v162, v84, v85
	v_add_f32_e32 v84, v84, v85
	v_add_f32_e32 v231, v80, v82
	v_exp_f32_e32 v86, v86
	v_exp_f32_e32 v87, v87
	s_waitcnt lgkmcnt(6)
	v_mfma_f32_32x32x16_f16 v[32:47], v[192:195], v[168:171], v[32:47]
	ds_read_b128 v[192:195], v226 offset:27648
	buffer_load_dwordx4 v[212:215], v252, s[4:7], s24 offen
	v_cvt_pk_f16_f32 v163, v86, v87
	v_add_f32_e32 v86, v86, v87
	v_add_f32_e32 v231, v231, v84
	v_exp_f32_e32 v88, v88
	v_exp_f32_e32 v89, v89
	v_mfma_f32_32x32x16_f16 v[48:63], v[196:199], v[168:171], v[48:63]
	ds_read_b128 v[196:199], v226 offset:32256
	v_cvt_pk_f16_f32 v164, v88, v89
	v_add_f32_e32 v88, v88, v89
	v_add_f32_e32 v231, v231, v86
	v_exp_f32_e32 v90, v90
	v_exp_f32_e32 v91, v91
	v_mfma_f32_32x32x16_f16 v[32:47], v[200:203], v[172:175], v[32:47]
	ds_read_b128 v[200:203], v226 offset:27680
	v_cvt_pk_f16_f32 v165, v90, v91
	v_add_f32_e32 v90, v90, v91
	v_add_f32_e32 v231, v231, v88
	v_exp_f32_e32 v92, v92
	v_exp_f32_e32 v93, v93
	v_mfma_f32_32x32x16_f16 v[48:63], v[204:207], v[172:175], v[48:63]
	ds_read_b128 v[204:207], v226 offset:32288
	v_cvt_pk_f16_f32 v166, v92, v93
	v_add_f32_e32 v92, v92, v93
	v_add_f32_e32 v231, v231, v90
	v_exp_f32_e32 v94, v94
	v_exp_f32_e32 v95, v95
	v_add_f32_e32 v231, v231, v92
	v_cvt_pk_f16_f32 v167, v94, v95
	v_add_f32_e32 v94, v94, v95
	v_add_f32_e32 v231, v231, v94
	v_cmp_nge_f32_e32 vcc, s34, v231
	s_cbranch_vccnz .Lovf_b1_30
.Lovfret_b1_30:
	v_add_f32_e32 v233, v233, v231
	s_waitcnt vmcnt(3)
	v_exp_f32_e32 v64, v64
	v_exp_f32_e32 v65, v65
	v_cvt_pk_f16_f32 v216, v216, v217
	v_cvt_pk_f16_f32 v217, v218, v219
	v_cvt_pk_f16_f32 v218, v220, v221
	v_cvt_pk_f16_f32 v219, v222, v223
	s_nop 0
	ds_write_b128 v228, v[216:219] offset:0
	v_cvt_pk_f16_f32 v168, v64, v65
	v_add_f32_e32 v64, v64, v65
	v_exp_f32_e32 v66, v66
	v_exp_f32_e32 v67, v67
	s_nop 0
	v_cvt_pk_f16_f32 v169, v66, v67
	v_add_f32_e32 v66, v66, v67
	v_exp_f32_e32 v68, v68
	v_exp_f32_e32 v69, v69
	s_nop 0
	buffer_load_dword v216, v230, s[4:7], s25 offen
	buffer_load_dword v217, v245, s[4:7], s25 offen
	v_cvt_pk_f16_f32 v170, v68, v69
	v_add_f32_e32 v68, v68, v69
	v_add_f32_e32 v231, v64, v66
	v_exp_f32_e32 v70, v70
	v_exp_f32_e32 v71, v71
	s_waitcnt lgkmcnt(1)
	v_mfma_f32_32x32x16_f16 v[32:47], v[192:195], v[160:163], v[32:47]
	ds_read_b128 v[192:195], v226 offset:27712
	buffer_load_dword v218, v246, s[4:7], s25 offen
	buffer_load_dword v219, v247, s[4:7], s25 offen
	v_cvt_pk_f16_f32 v171, v70, v71
	v_add_f32_e32 v70, v70, v71
	v_add_f32_e32 v231, v231, v68
	v_exp_f32_e32 v72, v72
	v_exp_f32_e32 v73, v73
	v_mfma_f32_32x32x16_f16 v[48:63], v[196:199], v[160:163], v[48:63]
	ds_read_b128 v[196:199], v226 offset:32320
	buffer_load_dword v220, v248, s[4:7], s25 offen
	buffer_load_dword v221, v249, s[4:7], s25 offen
	v_cvt_pk_f16_f32 v172, v72, v73
	v_add_f32_e32 v72, v72, v73
	v_add_f32_e32 v231, v231, v70
	v_exp_f32_e32 v74, v74
	v_exp_f32_e32 v75, v75
	v_mfma_f32_32x32x16_f16 v[32:47], v[200:203], v[164:167], v[32:47]
	ds_read_b128 v[200:203], v226 offset:27744
	buffer_load_dword v222, v250, s[4:7], s25 offen
	v_cvt_pk_f16_f32 v173, v74, v75
	v_add_f32_e32 v74, v74, v75
	v_add_f32_e32 v231, v231, v72
	v_exp_f32_e32 v76, v76
	v_exp_f32_e32 v77, v77
	v_mfma_f32_32x32x16_f16 v[48:63], v[204:207], v[164:167], v[48:63]
	ds_read_b128 v[204:207], v226 offset:32352
	buffer_load_dword v223, v251, s[4:7], s25 offen
	v_cvt_pk_f16_f32 v174, v76, v77
	v_add_f32_e32 v76, v76, v77
	v_add_f32_e32 v231, v231, v74
	v_exp_f32_e32 v78, v78
	v_exp_f32_e32 v79, v79
	v_add_f32_e32 v231, v231, v76
	v_cvt_pk_f16_f32 v175, v78, v79
	v_add_f32_e32 v78, v78, v79
	v_add_f32_e32 v231, v231, v78
	v_cmp_nge_f32_e32 vcc, s34, v231
	s_cbranch_vccnz .Lovf_b1_31
